# prologue issues x block A, then bank rows, then x block B (no early drain); fragment build in wait shadow; permlane softmax
# speedup vs baseline: 1.0161x; 1.0068x over previous
_Z12fused_kernelPKfS0_Pf:
	s_load_dwordx4 s[12:15], s[0:1], 0x0
	s_load_dwordx2 s[8:9], s[0:1], 0x10
	s_lshl_b32 s0, s2, 5
	s_and_b32 s0, s0, 0xe0
	s_lshr_b32 s3, s2, 3
	s_add_i32 s0, s0, s3
	v_and_b32_e32 v1, 63, v0
	v_lshrrev_b32_e32 v200, 6, v0
	s_lshl_b32 s0, s0, 17
	v_lshlrev_b32_e32 v194, 4, v0
	v_lshl_add_u32 v2, v200, 25, s0
	v_lshlrev_b32_e32 v198, 4, v1
	v_add_u32_e32 v106, 0x2000, v194
	v_add_u32_e32 v107, 0x4000, v194
	v_or_b32_e32 v203, v2, v198
	v_lshlrev_b32_e32 v196, 10, v200
	v_mov_b32_e32 v195, 0
	v_or_b32_e32 v233, v203, v196
	s_mov_b32 s7, 0x20000
	s_brev_b32 s6, 8
	s_waitcnt lgkmcnt(0)
	s_and_b32 s5, s13, 0xffff
	s_mov_b32 s4, s12
	buffer_load_dwordx4 v[70:73], v233, s[4:7], 0 offen nt
	v_or_b32_e32 v227, 0x2000, v233
	buffer_load_dwordx4 v[66:69], v227, s[4:7], 0 offen nt
	v_or_b32_e32 v226, 0x4000, v233
	buffer_load_dwordx4 v[78:81], v226, s[4:7], 0 offen nt
	v_or_b32_e32 v227, 0x6000, v233
	buffer_load_dwordx4 v[74:77], v227, s[4:7], 0 offen nt
	v_or_b32_e32 v226, 0x8000, v233
	buffer_load_dwordx4 v[86:89], v226, s[4:7], 0 offen nt
	v_or_b32_e32 v227, 0xa000, v233
	buffer_load_dwordx4 v[82:85], v227, s[4:7], 0 offen nt
	v_or_b32_e32 v226, 0xc000, v233
	buffer_load_dwordx4 v[94:97], v226, s[4:7], 0 offen nt
	v_or_b32_e32 v227, 0xe000, v233
	buffer_load_dwordx4 v[90:93], v227, s[4:7], 0 offen nt
	v_or_b32_e32 v226, 0x10000, v233
	buffer_load_dwordx4 v[150:153], v226, s[4:7], 0 offen nt
	v_or_b32_e32 v227, 0x12000, v233
	buffer_load_dwordx4 v[146:149], v227, s[4:7], 0 offen nt
	v_or_b32_e32 v226, 0x14000, v233
	buffer_load_dwordx4 v[162:165], v226, s[4:7], 0 offen nt
	v_or_b32_e32 v227, 0x16000, v233
	buffer_load_dwordx4 v[154:157], v227, s[4:7], 0 offen nt
	v_or_b32_e32 v226, 0x18000, v233
	buffer_load_dwordx4 v[174:177], v226, s[4:7], 0 offen nt
	v_or_b32_e32 v227, 0x1a000, v233
	buffer_load_dwordx4 v[166:169], v227, s[4:7], 0 offen nt
	v_or_b32_e32 v226, 0x1c000, v233
	buffer_load_dwordx4 v[182:185], v226, s[4:7], 0 offen nt
	v_or_b32_e32 v227, 0x1e000, v233
	buffer_load_dwordx4 v[178:181], v227, s[4:7], 0 offen nt
	global_load_dwordx4 v[228:231], v194, s[14:15]
	global_load_dwordx4 v[98:101], v106, s[14:15]
	global_load_dwordx4 v[102:105], v107, s[14:15]
	v_add_u32_e32 v107, 0x6000, v194
	global_load_dwordx4 v[116:119], v107, s[14:15]
	v_add_u32_e32 v106, 0x8000, v194
	global_load_dwordx4 v[120:123], v106, s[14:15]
	v_add_u32_e32 v107, 0xa000, v194
	global_load_dwordx4 v[124:127], v107, s[14:15]
	v_add_u32_e32 v106, 0xc000, v194
	global_load_dwordx4 v[128:131], v106, s[14:15]
	v_add_u32_e32 v107, 0xe000, v194
	global_load_dwordx4 v[132:135], v107, s[14:15]
	v_add_u32_e32 v106, 0x10000, v194
	global_load_dwordx4 v[136:139], v106, s[14:15]
	v_add_u32_e32 v107, 0x12000, v194
	global_load_dwordx4 v[140:143], v107, s[14:15]
	v_add_u32_e32 v106, 0x14000, v194
	global_load_dwordx4 v[158:161], v106, s[14:15]
	v_add_u32_e32 v107, 0x16000, v194
	global_load_dwordx4 v[170:173], v107, s[14:15]
	v_add_u32_e32 v106, 0x18000, v194
	global_load_dwordx4 v[186:189], v106, s[14:15]
	v_add_u32_e32 v107, 0x1a000, v194
	global_load_dwordx4 v[190:193], v107, s[14:15]
	v_add_u32_e32 v106, 0x1c000, v194
	global_load_dwordx4 v[204:207], v106, s[14:15]
	v_add_u32_e32 v107, 0x1e000, v194
	global_load_dwordx4 v[208:211], v107, s[14:15]
	v_add_u32_e32 v106, 0x20000, v194
	global_load_dwordx4 v[212:215], v106, s[14:15]
	v_add_u32_e32 v107, 0x22000, v194
	global_load_dwordx4 v[216:219], v107, s[14:15]
	v_add_u32_e32 v106, 0x24000, v194
	global_load_dwordx4 v[220:223], v106, s[14:15]
	v_add_u32_e32 v107, 0x26000, v194
	global_load_dwordx4 v[112:115], v107, s[14:15]
	v_add_u32_e32 v224, 0x400, v196
	s_movk_i32 s0, 0x1c00
	v_and_or_b32 v224, v224, s0, v203
	buffer_load_dwordx4 v[62:65], v224, s[4:7], 0 offen nt
	v_or_b32_e32 v227, 0x2000, v224
	buffer_load_dwordx4 v[38:41], v227, s[4:7], 0 offen nt
	v_or_b32_e32 v226, 0x4000, v224
	buffer_load_dwordx4 v[42:45], v226, s[4:7], 0 offen nt
	v_or_b32_e32 v227, 0x6000, v224
	buffer_load_dwordx4 v[14:17], v227, s[4:7], 0 offen nt
	v_or_b32_e32 v226, 0x8000, v224
	buffer_load_dwordx4 v[46:49], v226, s[4:7], 0 offen nt
	v_or_b32_e32 v227, 0xa000, v224
	buffer_load_dwordx4 v[18:21], v227, s[4:7], 0 offen nt
	v_or_b32_e32 v226, 0xc000, v224
	buffer_load_dwordx4 v[50:53], v226, s[4:7], 0 offen nt
	v_or_b32_e32 v227, 0xe000, v224
	buffer_load_dwordx4 v[22:25], v227, s[4:7], 0 offen nt
	v_or_b32_e32 v226, 0x10000, v224
	buffer_load_dwordx4 v[54:57], v226, s[4:7], 0 offen nt
	v_or_b32_e32 v227, 0x12000, v224
	buffer_load_dwordx4 v[26:29], v227, s[4:7], 0 offen nt
	v_or_b32_e32 v226, 0x14000, v224
	buffer_load_dwordx4 v[58:61], v226, s[4:7], 0 offen nt
	v_or_b32_e32 v227, 0x16000, v224
	buffer_load_dwordx4 v[30:33], v227, s[4:7], 0 offen nt
	v_or_b32_e32 v226, 0x18000, v224
	buffer_load_dwordx4 v[34:37], v226, s[4:7], 0 offen nt
	v_or_b32_e32 v227, 0x1a000, v224
	buffer_load_dwordx4 v[6:9], v227, s[4:7], 0 offen nt
	v_or_b32_e32 v226, 0x1c000, v224
	buffer_load_dwordx4 v[10:13], v226, s[4:7], 0 offen nt
	v_or_b32_e32 v227, 0x1e000, v224
	buffer_load_dwordx4 v[2:5], v227, s[4:7], 0 offen nt
	s_mov_b32 s1, 0xe000
	s_mov_b32 s10, 0xa000
	s_mov_b32 s11, 0x6000
	s_mov_b32 s12, 0xc000
	s_mov_b32 s13, 0x8000
	s_mov_b32 s14, 0x1e000
	s_mov_b32 s15, 0x1c000
	s_mov_b32 s16, 0x2000
	s_mov_b32 s17, 0x4000
	s_mov_b32 s18, 0x10000
	s_mov_b32 s19, 0x1a000
	s_mov_b32 s20, 0x18000
	s_mov_b32 s21, 0x16000
	s_mov_b32 s22, 0x14000
	s_mov_b32 s23, 0x12000
	s_mov_b32 s24, 0xe0
	s_mov_b32 s26, 0x3e13bb63
	v_lshrrev_b32_e32 v144, 3, v0
	v_bfe_u32 v145, v0, 1, 2
	v_lshlrev_b32_e32 v108, 3, v0
	v_and_b32_e32 v109, 8, v108
	v_lshlrev_b32_e32 v224, 8, v144
	v_lshlrev_b32_e32 v225, 6, v145
	v_lshlrev_b32_e32 v226, 8, v145
	v_lshlrev_b32_e32 v110, 10, v144
	v_or3_b32 v110, v226, v110, v109
	v_or3_b32 v111, v224, v225, v109
	v_add_u32_e32 v111, 0xff00, v111
	v_add_u32_e32 v144, 0x24800, v194
	v_bfe_u32 v201, v0, 4, 2
	v_and_b32_e32 v197, 15, v0
	v_lshlrev_b32_e32 v202, 2, v201
	s_waitcnt vmcnt(34)
	v_pk_add_f32 v[224:225], v[228:229], 0 op_sel_hi:[1,0]
	v_pk_add_f32 v[226:227], v[230:231], 0 op_sel_hi:[1,0]
	v_cvt_pk_bf16_f32 v228, v228, v229
	v_cvt_pk_bf16_f32 v229, v230, v231
	v_pk_add_f32 v[224:225], v[224:225], v[98:99]
	v_pk_add_f32 v[226:227], v[226:227], v[100:101]
	v_cvt_pk_bf16_f32 v98, v98, v99
	v_cvt_pk_bf16_f32 v99, v100, v101
	ds_write2_b64 v110, v[228:229], v[98:99] offset1:2
	s_waitcnt vmcnt(32)
	v_pk_add_f32 v[224:225], v[224:225], v[102:103]
	v_pk_add_f32 v[226:227], v[226:227], v[104:105]
	v_cvt_pk_bf16_f32 v102, v102, v103
	v_cvt_pk_bf16_f32 v103, v104, v105
	v_pk_add_f32 v[224:225], v[224:225], v[116:117]
	v_pk_add_f32 v[226:227], v[226:227], v[118:119]
	v_cvt_pk_bf16_f32 v116, v116, v117
	v_cvt_pk_bf16_f32 v117, v118, v119
	ds_write2_b64 v110, v[102:103], v[116:117] offset0:4 offset1:6
	s_waitcnt vmcnt(30)
	v_pk_add_f32 v[224:225], v[224:225], v[120:121]
	v_pk_add_f32 v[226:227], v[226:227], v[122:123]
	v_cvt_pk_bf16_f32 v120, v120, v121
	v_cvt_pk_bf16_f32 v121, v122, v123
	v_pk_add_f32 v[224:225], v[224:225], v[124:125]
	v_pk_add_f32 v[226:227], v[226:227], v[126:127]
	v_cvt_pk_bf16_f32 v124, v124, v125
	v_cvt_pk_bf16_f32 v125, v126, v127
	ds_write2_b64 v110, v[120:121], v[124:125] offset0:8 offset1:10
	s_waitcnt vmcnt(28)
	v_pk_add_f32 v[224:225], v[224:225], v[128:129]
	v_pk_add_f32 v[226:227], v[226:227], v[130:131]
	v_cvt_pk_bf16_f32 v128, v128, v129
	v_cvt_pk_bf16_f32 v129, v130, v131
	v_pk_add_f32 v[224:225], v[224:225], v[132:133]
	v_pk_add_f32 v[226:227], v[226:227], v[134:135]
	v_cvt_pk_bf16_f32 v132, v132, v133
	v_cvt_pk_bf16_f32 v133, v134, v135
	ds_write2_b64 v110, v[128:129], v[132:133] offset0:12 offset1:14
	s_waitcnt vmcnt(26)
	v_pk_add_f32 v[224:225], v[224:225], v[136:137]
	v_pk_add_f32 v[226:227], v[226:227], v[138:139]
	v_cvt_pk_bf16_f32 v136, v136, v137
	v_cvt_pk_bf16_f32 v137, v138, v139
	v_pk_add_f32 v[224:225], v[224:225], v[140:141]
	v_pk_add_f32 v[226:227], v[226:227], v[142:143]
	v_cvt_pk_bf16_f32 v140, v140, v141
	v_cvt_pk_bf16_f32 v141, v142, v143
	ds_write2_b64 v110, v[136:137], v[140:141] offset0:16 offset1:18
	s_waitcnt vmcnt(24)
	v_pk_add_f32 v[224:225], v[224:225], v[158:159]
	v_pk_add_f32 v[226:227], v[226:227], v[160:161]
	v_cvt_pk_bf16_f32 v158, v158, v159
	v_cvt_pk_bf16_f32 v159, v160, v161
	v_pk_add_f32 v[224:225], v[224:225], v[170:171]
	v_pk_add_f32 v[226:227], v[226:227], v[172:173]
	v_cvt_pk_bf16_f32 v170, v170, v171
	v_cvt_pk_bf16_f32 v171, v172, v173
	ds_write2_b64 v110, v[158:159], v[170:171] offset0:20 offset1:22
	s_waitcnt vmcnt(22)
	v_pk_add_f32 v[224:225], v[224:225], v[186:187]
	v_pk_add_f32 v[226:227], v[226:227], v[188:189]
	v_cvt_pk_bf16_f32 v186, v186, v187
	v_cvt_pk_bf16_f32 v187, v188, v189
	v_pk_add_f32 v[224:225], v[224:225], v[190:191]
	v_pk_add_f32 v[226:227], v[226:227], v[192:193]
	v_cvt_pk_bf16_f32 v190, v190, v191
	v_cvt_pk_bf16_f32 v191, v192, v193
	ds_write2_b64 v110, v[186:187], v[190:191] offset0:24 offset1:26
	s_waitcnt vmcnt(20)
	v_pk_add_f32 v[224:225], v[224:225], v[204:205]
	v_pk_add_f32 v[226:227], v[226:227], v[206:207]
	v_cvt_pk_bf16_f32 v204, v204, v205
	v_cvt_pk_bf16_f32 v205, v206, v207
	v_pk_add_f32 v[224:225], v[224:225], v[208:209]
	v_pk_add_f32 v[226:227], v[226:227], v[210:211]
	v_cvt_pk_bf16_f32 v208, v208, v209
	v_cvt_pk_bf16_f32 v209, v210, v211
	ds_write2_b64 v110, v[204:205], v[208:209] offset0:28 offset1:30
	s_waitcnt vmcnt(18)
	v_pk_add_f32 v[224:225], v[224:225], v[212:213]
	v_pk_add_f32 v[226:227], v[226:227], v[214:215]
	v_cvt_pk_bf16_f32 v212, v212, v213
	v_cvt_pk_bf16_f32 v213, v214, v215
	v_pk_add_f32 v[224:225], v[224:225], v[216:217]
	v_pk_add_f32 v[226:227], v[226:227], v[218:219]
	v_cvt_pk_bf16_f32 v216, v216, v217
	v_cvt_pk_bf16_f32 v217, v218, v219
	ds_write2_b64 v111, v[212:213], v[216:217] offset0:32 offset1:34
	s_waitcnt vmcnt(16)
	v_pk_add_f32 v[224:225], v[224:225], v[220:221]
	v_pk_add_f32 v[226:227], v[226:227], v[222:223]
	v_cvt_pk_bf16_f32 v220, v220, v221
	v_cvt_pk_bf16_f32 v221, v222, v223
	v_pk_add_f32 v[224:225], v[224:225], v[112:113]
	v_pk_add_f32 v[226:227], v[226:227], v[114:115]
	v_cvt_pk_bf16_f32 v112, v112, v113
	v_cvt_pk_bf16_f32 v113, v114, v115
	ds_write2_b64 v111, v[220:221], v[112:113] offset0:36 offset1:38
	v_pk_mul_f32 v[224:225], v[224:225], s[26:27] op_sel_hi:[1,0]
	v_pk_mul_f32 v[226:227], v[226:227], s[26:27] op_sel_hi:[1,0]
	ds_write_b128 v144, v[224:227]
	v_and_or_b32 v98, v0, 3, v202
	v_mov_b32_e32 v99, 0x10000
	v_lshl_or_b32 v204, v98, 4, v99
	s_movk_i32 s25, 0x2100
	v_mov_b32_e32 v98, 0x14000
	v_mad_u32_u24 v199, v200, s25, v98
	v_add_u32_e32 v98, 0x800, v196
	v_and_or_b32 v186, v98, s0, v203
	v_or_b32_e32 v98, 0x2000, v186
	s_waitcnt lgkmcnt(0)
	s_barrier
	buffer_load_dwordx4 v[102:105], v186, s[4:7], 0 offen nt
	s_nop 0
	buffer_load_dwordx4 v[98:101], v98, s[4:7], 0 offen nt
	v_or_b32_e32 v106, 0x4000, v186
	v_or_b32_e32 v107, 0x6000, v186
	v_or_b32_e32 v114, 0x8000, v186
	v_or_b32_e32 v115, 0xa000, v186
	v_or_b32_e32 v122, 0xc000, v186
	v_or_b32_e32 v123, 0xe000, v186
	v_or_b32_e32 v130, 0x10000, v186
	v_or_b32_e32 v131, 0x12000, v186
	v_or_b32_e32 v138, 0x14000, v186
	v_or_b32_e32 v139, 0x16000, v186
	v_or_b32_e32 v158, 0x18000, v186
	v_or_b32_e32 v159, 0x1a000, v186
	v_or_b32_e32 v187, 0x1c000, v186
	v_or_b32_e32 v186, 0x1e000, v186
	v_or_b32_e32 v213, v199, v109
	v_and_b32_e32 v214, 0x1f0, v108
	buffer_load_dwordx4 v[110:113], v106, s[4:7], 0 offen nt
	s_nop 0
	buffer_load_dwordx4 v[106:109], v107, s[4:7], 0 offen nt
	s_nop 0
	buffer_load_dwordx4 v[118:121], v114, s[4:7], 0 offen nt
	s_nop 0
	buffer_load_dwordx4 v[114:117], v115, s[4:7], 0 offen nt
	s_nop 0
	buffer_load_dwordx4 v[126:129], v122, s[4:7], 0 offen nt
	s_nop 0
	buffer_load_dwordx4 v[122:125], v123, s[4:7], 0 offen nt
	s_nop 0
	buffer_load_dwordx4 v[134:137], v130, s[4:7], 0 offen nt
	s_nop 0
	buffer_load_dwordx4 v[130:133], v131, s[4:7], 0 offen nt
	s_nop 0
	buffer_load_dwordx4 v[142:145], v138, s[4:7], 0 offen nt
	s_nop 0
	buffer_load_dwordx4 v[138:141], v139, s[4:7], 0 offen nt
	s_nop 0
	buffer_load_dwordx4 v[170:173], v158, s[4:7], 0 offen nt
	s_nop 0
	buffer_load_dwordx4 v[158:161], v159, s[4:7], 0 offen nt
	s_nop 0
	buffer_load_dwordx4 v[190:193], v187, s[4:7], 0 offen nt
	s_nop 0
	buffer_load_dwordx4 v[186:189], v186, s[4:7], 0 offen nt
	s_waitcnt vmcnt(32)
	v_cvt_pk_bf16_f32 v66, v66, v67
	v_cvt_pk_bf16_f32 v67, v68, v69
	s_movk_i32 s25, 0x50
	v_xad_u32 v207, v214, s25, v213
	s_movk_i32 s25, 0x60
	v_xad_u32 v206, v214, s25, v213
	s_movk_i32 s25, 0x70
	v_xad_u32 v205, v214, s25, v213
	s_movk_i32 s25, 0x80
	v_xad_u32 v211, v214, 16, v213
	v_xad_u32 v231, v214, s25, v213
	s_movk_i32 s25, 0x90
	v_xad_u32 v210, v214, 32, v213
	v_xad_u32 v230, v214, s25, v213
	s_movk_i32 s25, 0xa0
	ds_write_b64 v211, v[66:67] offset:512
	v_cvt_pk_bf16_f32 v66, v78, v79
	v_cvt_pk_bf16_f32 v67, v80, v81
	v_xad_u32 v209, v214, 48, v213
	v_xad_u32 v229, v214, s25, v213
	s_movk_i32 s25, 0xb0
	ds_write_b64 v210, v[66:67] offset:1024
	v_cvt_pk_bf16_f32 v66, v74, v75
	v_cvt_pk_bf16_f32 v67, v76, v77
	v_xad_u32 v208, v214, 64, v213
	v_xad_u32 v228, v214, s25, v213
	s_movk_i32 s25, 0xc0
	ds_write_b64 v209, v[66:67] offset:1536
	v_cvt_pk_bf16_f32 v66, v86, v87
	v_cvt_pk_bf16_f32 v67, v88, v89
	v_xad_u32 v227, v214, s25, v213
	s_movk_i32 s25, 0xd0
	v_xad_u32 v225, v214, s24, v213
	s_movk_i32 s24, 0xf0
	ds_write_b64 v208, v[66:67] offset:2048
	v_cvt_pk_bf16_f32 v66, v82, v83
	v_cvt_pk_bf16_f32 v67, v84, v85
	v_add_u32_e32 v212, v213, v214
	v_xad_u32 v226, v214, s25, v213
	v_xad_u32 v224, v214, s24, v213
	v_lshl_add_u32 v213, v197, 9, v199
	v_bitop3_b32 v214, v201, v0, 15 bitop3:0x78
	ds_write_b64 v207, v[66:67] offset:2560
	v_cvt_pk_bf16_f32 v66, v94, v95
	v_cvt_pk_bf16_f32 v67, v96, v97
	v_lshl_or_b32 v223, v214, 4, v213
	v_bitop3_b32 v214, v201, v197, 4 bitop3:0x36
	ds_write_b64 v206, v[66:67] offset:3072
	v_cvt_pk_bf16_f32 v66, v90, v91
	v_cvt_pk_bf16_f32 v67, v92, v93
	v_lshl_or_b32 v222, v214, 4, v213
	v_bitop3_b32 v214, v201, v197, 8 bitop3:0x36
	ds_write_b64 v205, v[66:67] offset:3584
	v_cvt_pk_bf16_f32 v66, v150, v151
	v_cvt_pk_bf16_f32 v67, v152, v153
	v_lshl_or_b32 v221, v214, 4, v213
	v_bitop3_b32 v214, v201, v197, 12 bitop3:0x36
	ds_write_b64 v231, v[66:67] offset:4096
	v_cvt_pk_bf16_f32 v66, v146, v147
	v_cvt_pk_bf16_f32 v67, v148, v149
	v_lshl_or_b32 v219, v214, 4, v213
	v_bitop3_b32 v214, v201, v197, 16 bitop3:0x36
	ds_write_b64 v230, v[66:67] offset:4608
	v_cvt_pk_bf16_f32 v66, v162, v163
	v_cvt_pk_bf16_f32 v67, v164, v165
	v_lshl_add_u32 v218, v214, 4, v213
	v_bitop3_b32 v214, v201, v197, 20 bitop3:0x36
	ds_write_b64 v229, v[66:67] offset:5120
	v_cvt_pk_bf16_f32 v66, v154, v155
	v_cvt_pk_bf16_f32 v67, v156, v157
	v_lshl_add_u32 v217, v214, 4, v213
	v_bitop3_b32 v214, v201, v197, 24 bitop3:0x36
	ds_write_b64 v228, v[66:67] offset:5632
	v_cvt_pk_bf16_f32 v66, v174, v175
	v_cvt_pk_bf16_f32 v67, v176, v177
	v_lshl_add_u32 v216, v214, 4, v213
	v_bitop3_b32 v214, v201, v197, 28 bitop3:0x36
	ds_write_b64 v227, v[66:67] offset:6144
	v_cvt_pk_bf16_f32 v66, v166, v167
	v_cvt_pk_bf16_f32 v67, v168, v169
	v_add_u32_e32 v235, 3, v200
	v_lshl_add_u32 v213, v214, 4, v213
	ds_write_b64 v226, v[66:67] offset:6656
	v_cvt_pk_bf16_f32 v66, v182, v183
	v_cvt_pk_bf16_f32 v67, v184, v185
	v_cvt_pk_bf16_f32 v70, v70, v71
	v_cvt_pk_bf16_f32 v71, v72, v73
	ds_write_b64 v212, v[70:71]
	ds_write_b64 v225, v[66:67] offset:7168
	v_cvt_pk_bf16_f32 v66, v178, v179
	v_cvt_pk_bf16_f32 v67, v180, v181
	ds_write_b64 v224, v[66:67] offset:7680
	v_lshl_or_b32 v66, v200, 13, v198
	ds_read_b128 v[66:69], v66
	v_lshlrev_b32_e32 v220, 11, v200
	v_or_b32_e32 v70, v204, v220
	ds_read_b128 v[70:73], v70
	ds_read_b128 v[74:77], v223
	v_lshlrev_b32_e32 v232, 3, v200
	v_or_b32_e32 v214, 1, v232
	s_waitcnt lgkmcnt(0)
	v_mfma_f32_16x16x32_bf16 v[70:73], v[70:73], v[74:77], 0
	v_lshlrev_b32_e32 v215, 8, v214
	v_or_b32_e32 v78, v204, v215
	v_or_b32_e32 v184, 2, v232
	v_mfma_f32_16x16x32_bf16 v[66:69], v[66:69], v[74:77], 0
	v_lshl_or_b32 v74, v214, 10, v198
	ds_read_b128 v[74:77], v74
	ds_read_b128 v[78:81], v78
	ds_read_b128 v[82:85], v222
	v_lshlrev_b32_e32 v185, 8, v184
	s_waitcnt lgkmcnt(0)
	v_mfma_f32_16x16x32_bf16 v[70:73], v[78:81], v[82:85], v[70:73]
	v_or_b32_e32 v78, v204, v185
	v_or_b32_e32 v182, 3, v232
	v_lshlrev_b32_e32 v183, 8, v182
	v_mfma_f32_16x16x32_bf16 v[66:69], v[74:77], v[82:85], v[66:69]
	v_lshl_or_b32 v74, v184, 10, v198
	ds_read_b128 v[74:77], v74
	ds_read_b128 v[78:81], v78
	ds_read_b128 v[82:85], v221
	s_waitcnt lgkmcnt(0)
	v_mfma_f32_16x16x32_bf16 v[70:73], v[78:81], v[82:85], v[70:73]
	v_or_b32_e32 v78, v204, v183
	v_or_b32_e32 v180, 4, v232
	v_lshlrev_b32_e32 v181, 8, v180
	v_mfma_f32_16x16x32_bf16 v[66:69], v[74:77], v[82:85], v[66:69]
	v_lshl_or_b32 v74, v182, 10, v198
	ds_read_b128 v[74:77], v74
	ds_read_b128 v[78:81], v78
	ds_read_b128 v[82:85], v219
	s_waitcnt lgkmcnt(0)
	v_mfma_f32_16x16x32_bf16 v[66:69], v[74:77], v[82:85], v[66:69]
	v_lshl_or_b32 v74, v180, 10, v198
	ds_read_b128 v[74:77], v74
	v_or_b32_e32 v178, 5, v232
	v_mfma_f32_16x16x32_bf16 v[70:73], v[78:81], v[82:85], v[70:73]
	v_or_b32_e32 v78, v204, v181
	ds_read_b128 v[78:81], v78
	ds_read_b128 v[82:85], v218
	v_lshlrev_b32_e32 v179, 8, v178
	s_waitcnt lgkmcnt(0)
	v_mfma_f32_16x16x32_bf16 v[66:69], v[74:77], v[82:85], v[66:69]
	v_lshl_or_b32 v74, v178, 10, v198
	ds_read_b128 v[74:77], v74
	v_or_b32_e32 v176, 6, v232
	v_mfma_f32_16x16x32_bf16 v[70:73], v[78:81], v[82:85], v[70:73]
	v_or_b32_e32 v78, v204, v179
	ds_read_b128 v[78:81], v78
	ds_read_b128 v[82:85], v217
	v_lshlrev_b32_e32 v177, 8, v176
	s_waitcnt lgkmcnt(0)
	v_mfma_f32_16x16x32_bf16 v[66:69], v[74:77], v[82:85], v[66:69]
	v_lshl_or_b32 v74, v176, 10, v198
	ds_read_b128 v[74:77], v74
	v_or_b32_e32 v174, 7, v232
	v_mfma_f32_16x16x32_bf16 v[70:73], v[78:81], v[82:85], v[70:73]
	v_or_b32_e32 v78, v204, v177
	ds_read_b128 v[78:81], v78
	ds_read_b128 v[82:85], v216
	v_lshlrev_b32_e32 v175, 8, v174
	s_waitcnt lgkmcnt(0)
	v_mfma_f32_16x16x32_bf16 v[66:69], v[74:77], v[82:85], v[66:69]
	v_lshl_or_b32 v74, v174, 10, v198
	s_waitcnt vmcnt(16)
	v_cvt_pk_bf16_f32 v14, v14, v15
	v_cvt_pk_bf16_f32 v15, v16, v17
	v_mfma_f32_16x16x32_bf16 v[70:73], v[78:81], v[82:85], v[70:73]
	v_or_b32_e32 v78, v204, v175
	ds_read_b128 v[74:77], v74
	ds_read_b128 v[78:81], v78
	ds_read_b128 v[82:85], v213
	ds_write_b64 v209, v[14:15] offset:1536
	v_cvt_pk_bf16_f32 v14, v46, v47
	v_cvt_pk_bf16_f32 v15, v48, v49
	ds_write_b64 v208, v[14:15] offset:2048
	v_cvt_pk_bf16_f32 v14, v18, v19
	v_cvt_pk_bf16_f32 v15, v20, v21
	ds_write_b64 v207, v[14:15] offset:2560
	v_cvt_pk_bf16_f32 v14, v50, v51
	v_cvt_pk_bf16_f32 v15, v52, v53
	ds_write_b64 v206, v[14:15] offset:3072
	v_cvt_pk_bf16_f32 v14, v22, v23
	v_cvt_pk_bf16_f32 v15, v24, v25
	ds_write_b64 v205, v[14:15] offset:3584
	v_cvt_pk_bf16_f32 v14, v54, v55
	v_cvt_pk_bf16_f32 v15, v56, v57
	v_cvt_pk_bf16_f32 v6, v6, v7
	v_cvt_pk_bf16_f32 v2, v2, v3
	ds_write_b64 v231, v[14:15] offset:4096
	v_cvt_pk_bf16_f32 v14, v26, v27
	v_cvt_pk_bf16_f32 v15, v28, v29
	v_cvt_pk_bf16_f32 v7, v8, v9
	ds_write_b64 v226, v[6:7] offset:6656
	v_cvt_pk_bf16_f32 v6, v10, v11
	v_cvt_pk_bf16_f32 v3, v4, v5
	ds_write_b64 v224, v[2:3] offset:7680
	v_lshlrev_b32_e32 v2, 10, v235
	ds_write_b64 v230, v[14:15] offset:4608
	v_cvt_pk_bf16_f32 v14, v58, v59
	v_cvt_pk_bf16_f32 v15, v60, v61
	v_cvt_pk_bf16_f32 v7, v12, v13
	ds_write_b64 v225, v[6:7] offset:7168
	v_and_or_b32 v6, v2, s0, v203
	ds_write_b64 v229, v[14:15] offset:5120
	v_cvt_pk_bf16_f32 v14, v30, v31
	v_cvt_pk_bf16_f32 v15, v32, v33
	v_or_b32_e32 v7, 0x2000, v6
	ds_write_b64 v228, v[14:15] offset:5632
	v_cvt_pk_bf16_f32 v14, v34, v35
	v_cvt_pk_bf16_f32 v15, v36, v37
	buffer_load_dwordx4 v[2:5], v6, s[4:7], 0 offen nt
	buffer_load_dwordx4 v[10:13], v7, s[4:7], 0 offen nt
	v_or_b32_e32 v7, 0x4000, v6
	ds_write_b64 v227, v[14:15] offset:6144
	buffer_load_dwordx4 v[14:17], v7, s[4:7], 0 offen nt
	v_or_b32_e32 v7, 0x6000, v6
	v_cvt_pk_bf16_f32 v38, v38, v39
	v_cvt_pk_bf16_f32 v39, v40, v41
	buffer_load_dwordx4 v[22:25], v7, s[4:7], 0 offen nt
	v_or_b32_e32 v7, 0x8000, v6
	ds_write_b64 v211, v[38:39] offset:512
	v_cvt_pk_bf16_f32 v38, v42, v43
	v_cvt_pk_bf16_f32 v39, v44, v45
	buffer_load_dwordx4 v[30:33], v7, s[4:7], 0 offen nt
	v_or_b32_e32 v7, 0xa000, v6
	ds_write_b64 v210, v[38:39] offset:1024
	buffer_load_dwordx4 v[38:41], v7, s[4:7], 0 offen nt
	v_or_b32_e32 v7, 0xc000, v6
	buffer_load_dwordx4 v[46:49], v7, s[4:7], 0 offen nt
	v_or_b32_e32 v7, 0xe000, v6
	v_cvt_pk_bf16_f32 v62, v62, v63
	v_cvt_pk_bf16_f32 v63, v64, v65
	buffer_load_dwordx4 v[54:57], v7, s[4:7], 0 offen nt
	v_or_b32_e32 v7, 0x10000, v6
	ds_write_b64 v212, v[62:63]
	buffer_load_dwordx4 v[62:65], v7, s[4:7], 0 offen nt
	v_or_b32_e32 v7, 0x12000, v6
	s_waitcnt lgkmcnt(14)
	v_mfma_f32_16x16x32_bf16 v[66:69], v[74:77], v[82:85], v[66:69]
	v_mfma_f32_16x16x32_bf16 v[74:77], v[78:81], v[82:85], v[70:73]
	s_nop 2
	buffer_load_dwordx4 v[70:73], v7, s[4:7], 0 offen nt
	v_or_b32_e32 v7, 0x14000, v6
	buffer_load_dwordx4 v[78:81], v7, s[4:7], 0 offen nt
	v_or_b32_e32 v7, 0x16000, v6
	buffer_load_dwordx4 v[86:89], v7, s[4:7], 0 offen nt
	v_or_b32_e32 v7, 0x18000, v6
	buffer_load_dwordx4 v[94:97], v7, s[4:7], 0 offen nt
	v_or_b32_e32 v7, 0x1a000, v6
	buffer_load_dwordx4 v[146:149], v7, s[4:7], 0 offen nt
	v_or_b32_e32 v7, 0x1c000, v6
	v_or_b32_e32 v6, 0x1e000, v6
	buffer_load_dwordx4 v[150:153], v7, s[4:7], 0 offen nt
	buffer_load_dwordx4 v[154:157], v6, s[4:7], 0 offen nt
	v_add_u32_e32 v6, 8, v232
	v_and_b32_e32 v50, 56, v6
	v_lshl_or_b32 v6, v50, 10, v198
	ds_read_b128 v[6:9], v6
	v_lshl_or_b32 v18, v50, 8, v204
	ds_read_b128 v[18:21], v18
	ds_read_b128 v[26:29], v223
	v_or_b32_e32 v34, 1, v50
	s_movk_i32 s24, 0x1000
	s_waitcnt lgkmcnt(0)
	v_mfma_f32_16x16x32_bf16 v[18:21], v[18:21], v[26:29], v[74:77]
	v_add_u32_e32 v234, 5, v200
	v_mfma_f32_16x16x32_bf16 v[6:9], v[6:9], v[26:29], v[66:69]
	v_lshl_or_b32 v26, v34, 10, v198
	ds_read_b128 v[26:29], v26
	v_lshl_or_b32 v34, v34, 8, v204
	ds_read_b128 v[34:37], v34
	ds_read_b128 v[42:45], v222
	s_waitcnt lgkmcnt(0)
	v_mfma_f32_16x16x32_bf16 v[18:21], v[34:37], v[42:45], v[18:21]
	v_or_b32_e32 v34, 2, v50
	v_mfma_f32_16x16x32_bf16 v[6:9], v[26:29], v[42:45], v[6:9]
	v_lshl_or_b32 v26, v34, 10, v198
	ds_read_b128 v[26:29], v26
	v_lshl_or_b32 v34, v34, 8, v204
	ds_read_b128 v[34:37], v34
	ds_read_b128 v[42:45], v221
	s_waitcnt lgkmcnt(0)
	v_mfma_f32_16x16x32_bf16 v[18:21], v[34:37], v[42:45], v[18:21]
	v_or_b32_e32 v34, 3, v50
	v_mfma_f32_16x16x32_bf16 v[6:9], v[26:29], v[42:45], v[6:9]
	v_lshl_or_b32 v26, v34, 10, v198
	ds_read_b128 v[26:29], v26
	v_lshl_or_b32 v34, v34, 8, v204
	ds_read_b128 v[34:37], v34
	ds_read_b128 v[42:45], v219
	s_waitcnt lgkmcnt(0)
	v_mfma_f32_16x16x32_bf16 v[18:21], v[34:37], v[42:45], v[18:21]
	v_or_b32_e32 v34, 4, v50
	v_mfma_f32_16x16x32_bf16 v[6:9], v[26:29], v[42:45], v[6:9]
	v_lshl_or_b32 v26, v34, 10, v198
	ds_read_b128 v[26:29], v26
	v_lshl_or_b32 v34, v34, 8, v204
	ds_read_b128 v[34:37], v34
	ds_read_b128 v[42:45], v218
	s_waitcnt lgkmcnt(0)
	v_mfma_f32_16x16x32_bf16 v[18:21], v[34:37], v[42:45], v[18:21]
	v_or_b32_e32 v34, 5, v50
	v_mfma_f32_16x16x32_bf16 v[6:9], v[26:29], v[42:45], v[6:9]
	v_lshl_or_b32 v26, v34, 10, v198
	ds_read_b128 v[26:29], v26
	v_lshl_or_b32 v34, v34, 8, v204
	ds_read_b128 v[34:37], v34
	ds_read_b128 v[42:45], v217
	s_waitcnt lgkmcnt(0)
	v_mfma_f32_16x16x32_bf16 v[18:21], v[34:37], v[42:45], v[18:21]
	v_or_b32_e32 v34, 6, v50
	v_mfma_f32_16x16x32_bf16 v[6:9], v[26:29], v[42:45], v[6:9]
	v_lshl_or_b32 v26, v34, 10, v198
	ds_read_b128 v[26:29], v26
	v_lshl_or_b32 v34, v34, 8, v204
	ds_read_b128 v[34:37], v34
	ds_read_b128 v[42:45], v216
	s_waitcnt lgkmcnt(0)
	v_mfma_f32_16x16x32_bf16 v[18:21], v[34:37], v[42:45], v[18:21]
	v_or_b32_e32 v34, 7, v50
	v_mfma_f32_16x16x32_bf16 v[6:9], v[26:29], v[42:45], v[6:9]
	v_lshl_or_b32 v26, v34, 10, v198
	ds_read_b128 v[26:29], v26
	v_lshl_or_b32 v34, v34, 8, v204
	ds_read_b128 v[34:37], v34
	ds_read_b128 v[42:45], v213
	s_waitcnt lgkmcnt(0)
	v_mfma_f32_16x16x32_bf16 v[162:165], v[26:29], v[42:45], v[6:9]
	s_waitcnt vmcnt(31)
	s_nop 1
	v_cvt_pk_bf16_f32 v6, v102, v103
	v_cvt_pk_bf16_f32 v7, v104, v105
	ds_write_b64 v212, v[6:7]
	s_waitcnt vmcnt(30)
	v_cvt_pk_bf16_f32 v6, v98, v99
	v_cvt_pk_bf16_f32 v7, v100, v101
	ds_write_b64 v211, v[6:7] offset:512
	s_waitcnt vmcnt(29)
	v_cvt_pk_bf16_f32 v6, v110, v111
	v_cvt_pk_bf16_f32 v7, v112, v113
	ds_write_b64 v210, v[6:7] offset:1024
	s_waitcnt vmcnt(28)
	v_cvt_pk_bf16_f32 v6, v106, v107
	v_cvt_pk_bf16_f32 v7, v108, v109
	ds_write_b64 v209, v[6:7] offset:1536
	s_waitcnt vmcnt(27)
	v_cvt_pk_bf16_f32 v6, v118, v119
	v_cvt_pk_bf16_f32 v7, v120, v121
	ds_write_b64 v208, v[6:7] offset:2048
	s_waitcnt vmcnt(26)
	v_cvt_pk_bf16_f32 v6, v114, v115
	v_cvt_pk_bf16_f32 v7, v116, v117
	ds_write_b64 v207, v[6:7] offset:2560
	s_waitcnt vmcnt(25)
	v_cvt_pk_bf16_f32 v6, v126, v127
	v_cvt_pk_bf16_f32 v7, v128, v129
	ds_write_b64 v206, v[6:7] offset:3072
	s_waitcnt vmcnt(24)
	v_cvt_pk_bf16_f32 v6, v122, v123
	v_cvt_pk_bf16_f32 v7, v124, v125
	ds_write_b64 v205, v[6:7] offset:3584
	s_waitcnt vmcnt(23)
	v_cvt_pk_bf16_f32 v6, v134, v135
	v_cvt_pk_bf16_f32 v7, v136, v137
	ds_write_b64 v231, v[6:7] offset:4096
	s_waitcnt vmcnt(22)
	v_cvt_pk_bf16_f32 v6, v130, v131
	v_cvt_pk_bf16_f32 v7, v132, v133
	ds_write_b64 v230, v[6:7] offset:4608
	s_waitcnt vmcnt(21)
	v_cvt_pk_bf16_f32 v6, v142, v143
	v_cvt_pk_bf16_f32 v7, v144, v145
	ds_write_b64 v229, v[6:7] offset:5120
	s_waitcnt vmcnt(20)
	v_cvt_pk_bf16_f32 v6, v138, v139
	v_cvt_pk_bf16_f32 v7, v140, v141
	ds_write_b64 v228, v[6:7] offset:5632
	s_waitcnt vmcnt(19)
	v_cvt_pk_bf16_f32 v6, v170, v171
	v_cvt_pk_bf16_f32 v7, v172, v173
	ds_write_b64 v227, v[6:7] offset:6144
	s_waitcnt vmcnt(18)
	v_cvt_pk_bf16_f32 v6, v158, v159
	v_mov_b32_e32 v106, 0x1000
	v_cvt_pk_bf16_f32 v7, v160, v161
	ds_write_b64 v226, v[6:7] offset:6656
	s_waitcnt vmcnt(17)
	v_cvt_pk_bf16_f32 v6, v190, v191
	v_bitop3_b32 v107, v233, s19, v106 bitop3:0xde
	v_mfma_f32_16x16x32_bf16 v[166:169], v[34:37], v[42:45], v[18:21]
	v_cvt_pk_bf16_f32 v7, v192, v193
	ds_write_b64 v225, v[6:7] offset:7168
	s_waitcnt vmcnt(16)
	v_cvt_pk_bf16_f32 v6, v186, v187
	v_bitop3_b32 v26, v233, s17, v106 bitop3:0xde
	v_bitop3_b32 v34, v233, s11, v106 bitop3:0xde
	v_bitop3_b32 v18, v233, s16, v106 bitop3:0xde
	v_bitop3_b32 v42, v233, s13, v106 bitop3:0xde
	v_bitop3_b32 v50, v233, s10, v106 bitop3:0xde
	v_bitop3_b32 v58, v233, s12, v106 bitop3:0xde
	v_bitop3_b32 v66, v233, s1, v106 bitop3:0xde
	v_bitop3_b32 v74, v233, s18, v106 bitop3:0xde
	v_bitop3_b32 v82, v233, s23, v106 bitop3:0xde
	v_bitop3_b32 v90, v233, s22, v106 bitop3:0xde
	v_bitop3_b32 v98, v233, s21, v106 bitop3:0xde
	v_bitop3_b32 v102, v233, s20, v106 bitop3:0xde
	buffer_load_dwordx4 v[110:113], v107, s[4:7], 0 offen nt
	v_bitop3_b32 v107, v233, s15, v106 bitop3:0xde
	v_bitop3_b32 v106, v233, s14, v106 bitop3:0xde
	v_cvt_pk_bf16_f32 v7, v188, v189
	ds_write_b64 v224, v[6:7] offset:7680
	v_bitop3_b32 v6, v203, s24, v196 bitop3:0x36
	buffer_load_dwordx4 v[42:45], v42, s[4:7], 0 offen nt
	s_nop 0
	buffer_load_dwordx4 v[50:53], v50, s[4:7], 0 offen nt
	s_nop 0
	buffer_load_dwordx4 v[58:61], v58, s[4:7], 0 offen nt
	s_nop 0
	buffer_load_dwordx4 v[66:69], v66, s[4:7], 0 offen nt
	s_nop 0
	buffer_load_dwordx4 v[74:77], v74, s[4:7], 0 offen nt
	s_nop 0
	buffer_load_dwordx4 v[82:85], v82, s[4:7], 0 offen nt
	s_nop 0
	buffer_load_dwordx4 v[90:93], v90, s[4:7], 0 offen nt
	s_nop 0
	buffer_load_dwordx4 v[98:101], v98, s[4:7], 0 offen nt
	s_nop 0
	buffer_load_dwordx4 v[102:105], v102, s[4:7], 0 offen nt
	s_nop 0
	buffer_load_dwordx4 v[126:129], v106, s[4:7], 0 offen nt
	buffer_load_dwordx4 v[118:121], v107, s[4:7], 0 offen nt
	s_nop 0
	buffer_load_dwordx4 v[6:9], v6, s[4:7], 0 offen nt
	s_nop 0
	buffer_load_dwordx4 v[18:21], v18, s[4:7], 0 offen nt
	s_nop 0
	buffer_load_dwordx4 v[26:29], v26, s[4:7], 0 offen nt
	s_nop 0
	buffer_load_dwordx4 v[34:37], v34, s[4:7], 0 offen nt
	v_add_u32_e32 v106, 16, v232
	v_and_b32_e32 v138, 56, v106
	v_lshl_or_b32 v106, v138, 10, v198
	ds_read_b128 v[106:109], v106
	v_lshl_or_b32 v114, v138, 8, v204
	ds_read_b128 v[114:117], v114
	ds_read_b128 v[122:125], v223
	v_or_b32_e32 v130, 1, v138
	s_waitcnt vmcnt(31)
	v_cvt_pk_bf16_f32 v2, v2, v3
	s_waitcnt lgkmcnt(0)
	v_mfma_f32_16x16x32_bf16 v[114:117], v[114:117], v[122:125], v[166:169]
	v_cvt_pk_bf16_f32 v3, v4, v5
	v_mfma_f32_16x16x32_bf16 v[106:109], v[106:109], v[122:125], v[162:165]
	v_lshl_or_b32 v122, v130, 10, v198
	ds_read_b128 v[122:125], v122
	v_lshl_or_b32 v130, v130, 8, v204
	ds_read_b128 v[130:133], v130
	ds_read_b128 v[134:137], v222
	s_waitcnt lgkmcnt(0)
	v_mfma_f32_16x16x32_bf16 v[114:117], v[130:133], v[134:137], v[114:117]
	v_or_b32_e32 v130, 2, v138
	v_mfma_f32_16x16x32_bf16 v[106:109], v[122:125], v[134:137], v[106:109]
	v_lshl_or_b32 v122, v130, 10, v198
	ds_read_b128 v[122:125], v122
	v_lshl_or_b32 v130, v130, 8, v204
	ds_read_b128 v[130:133], v130
	ds_read_b128 v[134:137], v221
	s_waitcnt lgkmcnt(0)
	v_mfma_f32_16x16x32_bf16 v[114:117], v[130:133], v[134:137], v[114:117]
	v_or_b32_e32 v130, 3, v138
	v_mfma_f32_16x16x32_bf16 v[106:109], v[122:125], v[134:137], v[106:109]
	v_lshl_or_b32 v122, v130, 10, v198
	ds_read_b128 v[122:125], v122
	v_lshl_or_b32 v130, v130, 8, v204
	ds_read_b128 v[130:133], v130
	ds_read_b128 v[134:137], v219
	s_waitcnt lgkmcnt(0)
	v_mfma_f32_16x16x32_bf16 v[114:117], v[130:133], v[134:137], v[114:117]
	v_or_b32_e32 v130, 4, v138
	v_mfma_f32_16x16x32_bf16 v[106:109], v[122:125], v[134:137], v[106:109]
	v_lshl_or_b32 v122, v130, 10, v198
	ds_read_b128 v[122:125], v122
	v_lshl_or_b32 v130, v130, 8, v204
	ds_read_b128 v[130:133], v130
	ds_read_b128 v[134:137], v218
	s_waitcnt lgkmcnt(0)
	v_mfma_f32_16x16x32_bf16 v[114:117], v[130:133], v[134:137], v[114:117]
	v_or_b32_e32 v130, 5, v138
	v_mfma_f32_16x16x32_bf16 v[106:109], v[122:125], v[134:137], v[106:109]
	v_lshl_or_b32 v122, v130, 10, v198
	ds_read_b128 v[122:125], v122
	v_lshl_or_b32 v130, v130, 8, v204
	ds_read_b128 v[130:133], v130
	ds_read_b128 v[134:137], v217
	s_waitcnt lgkmcnt(0)
	v_mfma_f32_16x16x32_bf16 v[114:117], v[130:133], v[134:137], v[114:117]
	v_or_b32_e32 v130, 6, v138
	v_mfma_f32_16x16x32_bf16 v[106:109], v[122:125], v[134:137], v[106:109]
	v_lshl_or_b32 v122, v130, 10, v198
	ds_read_b128 v[122:125], v122
	v_lshl_or_b32 v130, v130, 8, v204
	ds_read_b128 v[130:133], v130
	ds_read_b128 v[134:137], v216
	s_waitcnt lgkmcnt(0)
	v_mfma_f32_16x16x32_bf16 v[114:117], v[130:133], v[134:137], v[114:117]
	v_or_b32_e32 v130, 7, v138
	v_mfma_f32_16x16x32_bf16 v[106:109], v[122:125], v[134:137], v[106:109]
	v_lshl_or_b32 v122, v130, 10, v198
	v_lshl_or_b32 v130, v130, 8, v204
	ds_read_b128 v[122:125], v122
	ds_read_b128 v[134:137], v130
	ds_read_b128 v[138:141], v213
	ds_write_b64 v212, v[2:3]
	s_waitcnt vmcnt(30)
	v_cvt_pk_bf16_f32 v2, v10, v11
	v_cvt_pk_bf16_f32 v3, v12, v13
	ds_write_b64 v211, v[2:3] offset:512
	s_waitcnt vmcnt(29)
	v_cvt_pk_bf16_f32 v2, v14, v15
	v_cvt_pk_bf16_f32 v3, v16, v17
	ds_write_b64 v210, v[2:3] offset:1024
	s_waitcnt vmcnt(28)
	v_cvt_pk_bf16_f32 v2, v22, v23
	v_cvt_pk_bf16_f32 v3, v24, v25
	ds_write_b64 v209, v[2:3] offset:1536
	s_waitcnt vmcnt(27)
	v_cvt_pk_bf16_f32 v2, v30, v31
	v_cvt_pk_bf16_f32 v3, v32, v33
	ds_write_b64 v208, v[2:3] offset:2048
	s_waitcnt vmcnt(26)
	v_cvt_pk_bf16_f32 v2, v38, v39
	v_cvt_pk_bf16_f32 v3, v40, v41
	ds_write_b64 v207, v[2:3] offset:2560
	s_waitcnt vmcnt(25)
	v_cvt_pk_bf16_f32 v2, v46, v47
	v_cvt_pk_bf16_f32 v3, v48, v49
	ds_write_b64 v206, v[2:3] offset:3072
	s_waitcnt vmcnt(24)
	v_cvt_pk_bf16_f32 v2, v54, v55
	v_cvt_pk_bf16_f32 v3, v56, v57
	ds_write_b64 v205, v[2:3] offset:3584
	s_waitcnt vmcnt(23)
	v_cvt_pk_bf16_f32 v2, v62, v63
	v_cvt_pk_bf16_f32 v3, v64, v65
	ds_write_b64 v231, v[2:3] offset:4096
	s_waitcnt vmcnt(22)
	v_cvt_pk_bf16_f32 v2, v70, v71
	v_cvt_pk_bf16_f32 v3, v72, v73
	ds_write_b64 v230, v[2:3] offset:4608
	s_waitcnt vmcnt(21)
	v_cvt_pk_bf16_f32 v2, v78, v79
	v_cvt_pk_bf16_f32 v3, v80, v81
	ds_write_b64 v229, v[2:3] offset:5120
	s_waitcnt vmcnt(20)
	v_cvt_pk_bf16_f32 v2, v86, v87
	v_cvt_pk_bf16_f32 v3, v88, v89
	ds_write_b64 v228, v[2:3] offset:5632
	s_waitcnt vmcnt(19)
	v_cvt_pk_bf16_f32 v2, v94, v95
	v_cvt_pk_bf16_f32 v3, v96, v97
	ds_write_b64 v227, v[2:3] offset:6144
	s_waitcnt vmcnt(18)
	v_cvt_pk_bf16_f32 v2, v146, v147
	v_cvt_pk_bf16_f32 v3, v148, v149
	ds_write_b64 v226, v[2:3] offset:6656
	s_waitcnt vmcnt(17)
	v_cvt_pk_bf16_f32 v2, v150, v151
	v_cvt_pk_bf16_f32 v3, v152, v153
	ds_write_b64 v225, v[2:3] offset:7168
	s_waitcnt vmcnt(16)
	v_cvt_pk_bf16_f32 v2, v154, v155
	v_cvt_pk_bf16_f32 v3, v156, v157
	ds_write_b64 v224, v[2:3] offset:7680
	v_lshlrev_b32_e32 v2, 10, v234
	s_waitcnt lgkmcnt(14)
	v_mfma_f32_16x16x32_bf16 v[130:133], v[122:125], v[138:141], v[106:109]
	v_and_or_b32 v122, v2, s0, v203
	buffer_load_dwordx4 v[2:5], v122, s[4:7], 0 offen nt
	v_or_b32_e32 v10, 0x2000, v122
	v_mfma_f32_16x16x32_bf16 v[134:137], v[134:137], v[138:141], v[114:117]
	v_or_b32_e32 v14, 0x4000, v122
	v_or_b32_e32 v22, 0x6000, v122
	v_or_b32_e32 v30, 0x8000, v122
	v_or_b32_e32 v38, 0xa000, v122
	v_or_b32_e32 v46, 0xc000, v122
	v_or_b32_e32 v54, 0xe000, v122
	v_or_b32_e32 v62, 0x10000, v122
	v_or_b32_e32 v70, 0x12000, v122
	v_or_b32_e32 v78, 0x14000, v122
	v_or_b32_e32 v86, 0x16000, v122
	v_or_b32_e32 v94, 0x18000, v122
	v_or_b32_e32 v106, 0x1a000, v122
	v_or_b32_e32 v114, 0x1c000, v122
	v_or_b32_e32 v122, 0x1e000, v122
	buffer_load_dwordx4 v[54:57], v54, s[4:7], 0 offen nt
	s_nop 0
	buffer_load_dwordx4 v[62:65], v62, s[4:7], 0 offen nt
	s_nop 0
	buffer_load_dwordx4 v[70:73], v70, s[4:7], 0 offen nt
	s_nop 0
	buffer_load_dwordx4 v[78:81], v78, s[4:7], 0 offen nt
	s_nop 0
	buffer_load_dwordx4 v[86:89], v86, s[4:7], 0 offen nt
	s_nop 0
	buffer_load_dwordx4 v[94:97], v94, s[4:7], 0 offen nt
	s_nop 0
	buffer_load_dwordx4 v[106:109], v106, s[4:7], 0 offen nt
	s_nop 0
	buffer_load_dwordx4 v[114:117], v114, s[4:7], 0 offen nt
	s_nop 0
	buffer_load_dwordx4 v[122:125], v122, s[4:7], 0 offen nt
	s_nop 0
	buffer_load_dwordx4 v[10:13], v10, s[4:7], 0 offen nt
	s_nop 0
	buffer_load_dwordx4 v[14:17], v14, s[4:7], 0 offen nt
	s_nop 0
	buffer_load_dwordx4 v[22:25], v22, s[4:7], 0 offen nt
	s_nop 0
	buffer_load_dwordx4 v[30:33], v30, s[4:7], 0 offen nt
	s_nop 0
	buffer_load_dwordx4 v[38:41], v38, s[4:7], 0 offen nt
	s_nop 0
	buffer_load_dwordx4 v[46:49], v46, s[4:7], 0 offen nt
	v_lshlrev_b32_e32 v138, 3, v235
	v_and_b32_e32 v150, 56, v138
	v_lshl_or_b32 v138, v150, 10, v198
	ds_read_b128 v[138:141], v138
	v_lshl_or_b32 v142, v150, 8, v204
	ds_read_b128 v[142:145], v142
	ds_read_b128 v[146:149], v223
	s_waitcnt vmcnt(19)
	v_cvt_pk_bf16_f32 v6, v6, v7
	v_cvt_pk_bf16_f32 v7, v8, v9
	s_waitcnt lgkmcnt(0)
	v_mfma_f32_16x16x32_bf16 v[134:137], v[142:145], v[146:149], v[134:137]
	v_or_b32_e32 v142, 1, v150
	v_mfma_f32_16x16x32_bf16 v[130:133], v[138:141], v[146:149], v[130:133]
	v_lshl_or_b32 v138, v142, 10, v198
	ds_read_b128 v[138:141], v138
	v_lshl_or_b32 v142, v142, 8, v204
	ds_read_b128 v[142:145], v142
	ds_read_b128 v[146:149], v222
	s_waitcnt lgkmcnt(0)
	v_mfma_f32_16x16x32_bf16 v[134:137], v[142:145], v[146:149], v[134:137]
	v_or_b32_e32 v142, 2, v150
	v_mfma_f32_16x16x32_bf16 v[130:133], v[138:141], v[146:149], v[130:133]
	v_lshl_or_b32 v138, v142, 10, v198
	ds_read_b128 v[138:141], v138
	v_lshl_or_b32 v142, v142, 8, v204
	ds_read_b128 v[142:145], v142
	ds_read_b128 v[146:149], v221
	s_waitcnt lgkmcnt(0)
	v_mfma_f32_16x16x32_bf16 v[134:137], v[142:145], v[146:149], v[134:137]
	v_or_b32_e32 v142, 3, v150
	v_mfma_f32_16x16x32_bf16 v[130:133], v[138:141], v[146:149], v[130:133]
	v_lshl_or_b32 v138, v142, 10, v198
	ds_read_b128 v[138:141], v138
	v_lshl_or_b32 v142, v142, 8, v204
	ds_read_b128 v[142:145], v142
	ds_read_b128 v[146:149], v219
	s_waitcnt lgkmcnt(0)
	v_mfma_f32_16x16x32_bf16 v[134:137], v[142:145], v[146:149], v[134:137]
	v_or_b32_e32 v142, 4, v150
	v_mfma_f32_16x16x32_bf16 v[130:133], v[138:141], v[146:149], v[130:133]
	v_lshl_or_b32 v138, v142, 10, v198
	ds_read_b128 v[138:141], v138
	v_lshl_or_b32 v142, v142, 8, v204
	ds_read_b128 v[142:145], v142
	ds_read_b128 v[146:149], v218
	s_waitcnt lgkmcnt(0)
	v_mfma_f32_16x16x32_bf16 v[134:137], v[142:145], v[146:149], v[134:137]
	v_or_b32_e32 v142, 5, v150
	v_mfma_f32_16x16x32_bf16 v[130:133], v[138:141], v[146:149], v[130:133]
	v_lshl_or_b32 v138, v142, 10, v198
	ds_read_b128 v[138:141], v138
	v_lshl_or_b32 v142, v142, 8, v204
	ds_read_b128 v[142:145], v142
	ds_read_b128 v[146:149], v217
	s_waitcnt lgkmcnt(0)
	v_mfma_f32_16x16x32_bf16 v[134:137], v[142:145], v[146:149], v[134:137]
	v_or_b32_e32 v142, 6, v150
	v_mfma_f32_16x16x32_bf16 v[130:133], v[138:141], v[146:149], v[130:133]
	v_lshl_or_b32 v138, v142, 10, v198
	ds_read_b128 v[138:141], v138
	v_lshl_or_b32 v142, v142, 8, v204
	ds_read_b128 v[142:145], v142
	ds_read_b128 v[146:149], v216
	s_waitcnt lgkmcnt(0)
	v_mfma_f32_16x16x32_bf16 v[134:137], v[142:145], v[146:149], v[134:137]
	v_or_b32_e32 v142, 7, v150
	v_mfma_f32_16x16x32_bf16 v[130:133], v[138:141], v[146:149], v[130:133]
	v_lshl_or_b32 v138, v142, 10, v198
	v_lshl_or_b32 v142, v142, 8, v204
	ds_read_b128 v[138:141], v138
	ds_read_b128 v[142:145], v142
	ds_read_b128 v[146:149], v213
	ds_write_b64 v212, v[6:7]
	s_waitcnt vmcnt(18)
	v_cvt_pk_bf16_f32 v6, v18, v19
	v_cvt_pk_bf16_f32 v7, v20, v21
	ds_write_b64 v211, v[6:7] offset:512
	s_waitcnt vmcnt(17)
	v_cvt_pk_bf16_f32 v6, v26, v27
	v_cvt_pk_bf16_f32 v7, v28, v29
	ds_write_b64 v210, v[6:7] offset:1024
	s_waitcnt vmcnt(16)
	v_cvt_pk_bf16_f32 v6, v34, v35
	v_cvt_pk_bf16_f32 v7, v36, v37
	ds_write_b64 v209, v[6:7] offset:1536
	v_cvt_pk_bf16_f32 v6, v42, v43
	v_cvt_pk_bf16_f32 v7, v44, v45
	ds_write_b64 v208, v[6:7] offset:2048
	v_cvt_pk_bf16_f32 v6, v50, v51
	v_cvt_pk_bf16_f32 v7, v52, v53
	ds_write_b64 v207, v[6:7] offset:2560
	v_cvt_pk_bf16_f32 v6, v58, v59
	v_cvt_pk_bf16_f32 v7, v60, v61
	ds_write_b64 v206, v[6:7] offset:3072
	v_cvt_pk_bf16_f32 v6, v66, v67
	v_cvt_pk_bf16_f32 v7, v68, v69
	ds_write_b64 v205, v[6:7] offset:3584
	v_cvt_pk_bf16_f32 v6, v74, v75
	v_cvt_pk_bf16_f32 v7, v76, v77
	ds_write_b64 v231, v[6:7] offset:4096
	v_cvt_pk_bf16_f32 v6, v82, v83
	v_cvt_pk_bf16_f32 v7, v84, v85
	ds_write_b64 v230, v[6:7] offset:4608
	v_cvt_pk_bf16_f32 v6, v90, v91
	v_cvt_pk_bf16_f32 v7, v92, v93
	ds_write_b64 v229, v[6:7] offset:5120
	v_cvt_pk_bf16_f32 v6, v98, v99
	v_cvt_pk_bf16_f32 v7, v100, v101
	ds_write_b64 v228, v[6:7] offset:5632
	v_cvt_pk_bf16_f32 v6, v102, v103
	v_cvt_pk_bf16_f32 v7, v104, v105
	ds_write_b64 v227, v[6:7] offset:6144
	v_cvt_pk_bf16_f32 v6, v110, v111
	v_cvt_pk_bf16_f32 v7, v112, v113
	ds_write_b64 v226, v[6:7] offset:6656
	v_cvt_pk_bf16_f32 v6, v118, v119
	v_cvt_pk_bf16_f32 v7, v120, v121
	ds_write_b64 v225, v[6:7] offset:7168
	v_cvt_pk_bf16_f32 v6, v126, v127
	v_cvt_pk_bf16_f32 v7, v128, v129
	ds_write_b64 v224, v[6:7] offset:7680
	v_add_u32_e32 v6, 0x1800, v196
	v_and_or_b32 v126, v6, s0, v203
	buffer_load_dwordx4 v[6:9], v126, s[4:7], 0 offen nt
	v_or_b32_e32 v18, 0x2000, v126
	v_or_b32_e32 v26, 0x4000, v126
	v_or_b32_e32 v34, 0x6000, v126
	v_or_b32_e32 v42, 0x8000, v126
	v_or_b32_e32 v50, 0xa000, v126
	v_or_b32_e32 v58, 0xc000, v126
	v_or_b32_e32 v66, 0xe000, v126
	v_or_b32_e32 v74, 0x10000, v126
	v_or_b32_e32 v82, 0x12000, v126
	v_or_b32_e32 v90, 0x14000, v126
	v_or_b32_e32 v98, 0x16000, v126
	v_or_b32_e32 v102, 0x18000, v126
	v_or_b32_e32 v110, 0x1a000, v126
	v_or_b32_e32 v118, 0x1c000, v126
	v_or_b32_e32 v126, 0x1e000, v126
	buffer_load_dwordx4 v[50:53], v50, s[4:7], 0 offen nt
	s_waitcnt lgkmcnt(14)
	v_mfma_f32_16x16x32_bf16 v[130:133], v[138:141], v[146:149], v[130:133]
	buffer_load_dwordx4 v[58:61], v58, s[4:7], 0 offen nt
	s_nop 0
	buffer_load_dwordx4 v[66:69], v66, s[4:7], 0 offen nt
	v_mfma_f32_16x16x32_bf16 v[134:137], v[142:145], v[146:149], v[134:137]
	buffer_load_dwordx4 v[74:77], v74, s[4:7], 0 offen nt
	v_add_u32_e32 v142, 7, v200
	buffer_load_dwordx4 v[82:85], v82, s[4:7], 0 offen nt
	s_nop 0
	buffer_load_dwordx4 v[90:93], v90, s[4:7], 0 offen nt
	s_nop 0
	buffer_load_dwordx4 v[98:101], v98, s[4:7], 0 offen nt
	s_nop 0
	buffer_load_dwordx4 v[102:105], v102, s[4:7], 0 offen nt
	s_nop 0
	buffer_load_dwordx4 v[110:113], v110, s[4:7], 0 offen nt
	s_nop 0
	buffer_load_dwordx4 v[118:121], v118, s[4:7], 0 offen nt
	s_nop 0
	buffer_load_dwordx4 v[126:129], v126, s[4:7], 0 offen nt
	s_nop 0
	buffer_load_dwordx4 v[18:21], v18, s[4:7], 0 offen nt
	s_nop 0
	buffer_load_dwordx4 v[26:29], v26, s[4:7], 0 offen nt
	s_nop 0
	buffer_load_dwordx4 v[34:37], v34, s[4:7], 0 offen nt
	s_nop 0
	buffer_load_dwordx4 v[42:45], v42, s[4:7], 0 offen nt
	v_xor_b32_e32 v143, 32, v232
	v_lshl_or_b32 v138, v143, 10, v198
	ds_read_b128 v[138:141], v138
	v_lshl_or_b32 v143, v143, 8, v204
	ds_read_b128 v[144:147], v143
	ds_read_b128 v[148:151], v223
	v_bitop3_b32 v143, v232, 1, 32 bitop3:0xde
	s_waitcnt vmcnt(31)
	v_cvt_pk_bf16_f32 v2, v2, v3
	s_waitcnt lgkmcnt(0)
	v_mfma_f32_16x16x32_bf16 v[134:137], v[144:147], v[148:151], v[134:137]
	v_cvt_pk_bf16_f32 v3, v4, v5
	v_mfma_f32_16x16x32_bf16 v[130:133], v[138:141], v[148:151], v[130:133]
	v_lshl_or_b32 v138, v143, 10, v198
	ds_read_b128 v[138:141], v138
	v_lshl_or_b32 v143, v143, 8, v204
	ds_read_b128 v[144:147], v143
	ds_read_b128 v[148:151], v222
	v_bitop3_b32 v143, v232, 2, 32 bitop3:0xde
	s_waitcnt lgkmcnt(0)
	v_mfma_f32_16x16x32_bf16 v[134:137], v[144:147], v[148:151], v[134:137]
	v_mfma_f32_16x16x32_bf16 v[130:133], v[138:141], v[148:151], v[130:133]
	v_lshl_or_b32 v138, v143, 10, v198
	ds_read_b128 v[138:141], v138
	v_lshl_or_b32 v143, v143, 8, v204
	ds_read_b128 v[144:147], v143
	ds_read_b128 v[148:151], v221
	v_bitop3_b32 v143, v232, 3, 32 bitop3:0xde
	s_waitcnt lgkmcnt(0)
	v_mfma_f32_16x16x32_bf16 v[130:133], v[138:141], v[148:151], v[130:133]
	v_lshl_or_b32 v138, v143, 10, v198
	ds_read_b128 v[138:141], v138
	v_lshl_or_b32 v143, v143, 8, v204
	v_mfma_f32_16x16x32_bf16 v[134:137], v[144:147], v[148:151], v[134:137]
	ds_read_b128 v[144:147], v143
	ds_read_b128 v[148:151], v219
	v_bitop3_b32 v143, v232, 4, 32 bitop3:0xde
	s_waitcnt lgkmcnt(0)
	v_mfma_f32_16x16x32_bf16 v[130:133], v[138:141], v[148:151], v[130:133]
	v_lshl_or_b32 v138, v143, 10, v198
	ds_read_b128 v[138:141], v138
	v_lshl_or_b32 v143, v143, 8, v204
	v_mfma_f32_16x16x32_bf16 v[134:137], v[144:147], v[148:151], v[134:137]
	ds_read_b128 v[144:147], v143
	ds_read_b128 v[148:151], v218
	v_bitop3_b32 v143, v232, 5, 32 bitop3:0xde
	s_waitcnt lgkmcnt(0)
	v_mfma_f32_16x16x32_bf16 v[130:133], v[138:141], v[148:151], v[130:133]
	v_lshl_or_b32 v138, v143, 10, v198
	ds_read_b128 v[138:141], v138
	v_lshl_or_b32 v143, v143, 8, v204
	v_mfma_f32_16x16x32_bf16 v[134:137], v[144:147], v[148:151], v[134:137]
	ds_read_b128 v[144:147], v143
	ds_read_b128 v[148:151], v217
	v_bitop3_b32 v143, v232, 6, 32 bitop3:0xde
	s_waitcnt lgkmcnt(0)
	v_mfma_f32_16x16x32_bf16 v[130:133], v[138:141], v[148:151], v[130:133]
	v_lshl_or_b32 v138, v143, 10, v198
	ds_read_b128 v[138:141], v138
	v_lshl_or_b32 v143, v143, 8, v204
	v_mfma_f32_16x16x32_bf16 v[134:137], v[144:147], v[148:151], v[134:137]
	ds_read_b128 v[144:147], v143
	ds_read_b128 v[148:151], v216
	v_bitop3_b32 v143, v232, 7, 32 bitop3:0xde
	s_waitcnt lgkmcnt(0)
	v_mfma_f32_16x16x32_bf16 v[130:133], v[138:141], v[148:151], v[130:133]
	v_lshl_or_b32 v138, v143, 10, v198
	v_lshl_or_b32 v143, v143, 8, v204
	ds_read_b128 v[138:141], v138
	v_mfma_f32_16x16x32_bf16 v[134:137], v[144:147], v[148:151], v[134:137]
	ds_read_b128 v[144:147], v143
	ds_read_b128 v[148:151], v213
	ds_write_b64 v212, v[2:3]
	s_waitcnt vmcnt(21)
	v_cvt_pk_bf16_f32 v2, v10, v11
	v_cvt_pk_bf16_f32 v3, v12, v13
	ds_write_b64 v211, v[2:3] offset:512
	s_waitcnt vmcnt(20)
	v_cvt_pk_bf16_f32 v2, v14, v15
	v_cvt_pk_bf16_f32 v3, v16, v17
	ds_write_b64 v210, v[2:3] offset:1024
	s_waitcnt vmcnt(19)
	v_cvt_pk_bf16_f32 v2, v22, v23
	v_cvt_pk_bf16_f32 v3, v24, v25
	ds_write_b64 v209, v[2:3] offset:1536
	s_waitcnt vmcnt(18)
	v_cvt_pk_bf16_f32 v2, v30, v31
	v_cvt_pk_bf16_f32 v3, v32, v33
	ds_write_b64 v208, v[2:3] offset:2048
	s_waitcnt vmcnt(17)
	v_cvt_pk_bf16_f32 v2, v38, v39
	v_cvt_pk_bf16_f32 v3, v40, v41
	ds_write_b64 v207, v[2:3] offset:2560
	s_waitcnt vmcnt(16)
	v_cvt_pk_bf16_f32 v2, v46, v47
	v_cvt_pk_bf16_f32 v3, v48, v49
	ds_write_b64 v206, v[2:3] offset:3072
	v_cvt_pk_bf16_f32 v2, v54, v55
	v_cvt_pk_bf16_f32 v3, v56, v57
	ds_write_b64 v205, v[2:3] offset:3584
	v_cvt_pk_bf16_f32 v2, v62, v63
	v_cvt_pk_bf16_f32 v3, v64, v65
	ds_write_b64 v231, v[2:3] offset:4096
	v_cvt_pk_bf16_f32 v2, v70, v71
	v_cvt_pk_bf16_f32 v3, v72, v73
	ds_write_b64 v230, v[2:3] offset:4608
	v_cvt_pk_bf16_f32 v2, v78, v79
	v_cvt_pk_bf16_f32 v3, v80, v81
	ds_write_b64 v229, v[2:3] offset:5120
	v_cvt_pk_bf16_f32 v2, v86, v87
	v_cvt_pk_bf16_f32 v3, v88, v89
	ds_write_b64 v228, v[2:3] offset:5632
	v_cvt_pk_bf16_f32 v2, v94, v95
	v_cvt_pk_bf16_f32 v3, v96, v97
	ds_write_b64 v227, v[2:3] offset:6144
	v_cvt_pk_bf16_f32 v2, v106, v107
	v_cvt_pk_bf16_f32 v3, v108, v109
	ds_write_b64 v226, v[2:3] offset:6656
	v_cvt_pk_bf16_f32 v2, v114, v115
	v_cvt_pk_bf16_f32 v3, v116, v117
	ds_write_b64 v225, v[2:3] offset:7168
	v_cvt_pk_bf16_f32 v2, v122, v123
	v_cvt_pk_bf16_f32 v3, v124, v125
	ds_write_b64 v224, v[2:3] offset:7680
	v_lshlrev_b32_e32 v2, 10, v142
	v_and_or_b32 v2, v2, s0, v203
	v_or_b32_e32 v3, 0x2000, v2
	buffer_load_dwordx4 v[10:13], v2, s[4:7], 0 offen nt
	buffer_load_dwordx4 v[14:17], v3, s[4:7], 0 offen nt
	v_or_b32_e32 v3, 0x4000, v2
	buffer_load_dwordx4 v[22:25], v3, s[4:7], 0 offen nt
	v_or_b32_e32 v3, 0x6000, v2
	buffer_load_dwordx4 v[30:33], v3, s[4:7], 0 offen nt
	v_or_b32_e32 v3, 0x8000, v2
	buffer_load_dwordx4 v[38:41], v3, s[4:7], 0 offen nt
	v_or_b32_e32 v3, 0xa000, v2
	buffer_load_dwordx4 v[46:49], v3, s[4:7], 0 offen nt
	v_or_b32_e32 v3, 0xc000, v2
	buffer_load_dwordx4 v[54:57], v3, s[4:7], 0 offen nt
	v_or_b32_e32 v3, 0xe000, v2
	buffer_load_dwordx4 v[62:65], v3, s[4:7], 0 offen nt
	v_or_b32_e32 v3, 0x10000, v2
	buffer_load_dwordx4 v[70:73], v3, s[4:7], 0 offen nt
	v_or_b32_e32 v3, 0x12000, v2
	buffer_load_dwordx4 v[78:81], v3, s[4:7], 0 offen nt
	v_or_b32_e32 v3, 0x14000, v2
	buffer_load_dwordx4 v[86:89], v3, s[4:7], 0 offen nt
	v_or_b32_e32 v3, 0x16000, v2
	buffer_load_dwordx4 v[94:97], v3, s[4:7], 0 offen nt
	v_or_b32_e32 v3, 0x18000, v2
	buffer_load_dwordx4 v[106:109], v3, s[4:7], 0 offen nt
	v_or_b32_e32 v3, 0x1a000, v2
	buffer_load_dwordx4 v[114:117], v3, s[4:7], 0 offen nt
	v_or_b32_e32 v3, 0x1c000, v2
	v_or_b32_e32 v2, 0x1e000, v2
	s_waitcnt lgkmcnt(14)
	v_mfma_f32_16x16x32_bf16 v[138:141], v[138:141], v[148:151], v[130:133]
	buffer_load_dwordx4 v[122:125], v3, s[4:7], 0 offen nt
	s_nop 1
	buffer_load_dwordx4 v[130:133], v2, s[4:7], 0 offen nt
	v_mfma_f32_16x16x32_bf16 v[134:137], v[144:147], v[148:151], v[134:137]
	v_lshlrev_b32_e32 v2, 3, v234
	v_and_b32_e32 v143, 56, v2
	v_lshl_or_b32 v2, v143, 10, v198
	v_lshl_or_b32 v152, v143, 8, v204
	ds_read_b128 v[2:5], v2
	ds_read_b128 v[144:147], v223
	ds_read_b128 v[148:151], v222
	ds_read_b128 v[152:155], v152
	v_or_b32_e32 v156, 1, v143
	v_lshl_or_b32 v157, v156, 10, v198
	s_waitcnt lgkmcnt(2)
	v_mfma_f32_16x16x32_bf16 v[2:5], v[2:5], v[144:147], v[138:141]
	s_waitcnt vmcnt(31)
	v_cvt_pk_bf16_f32 v6, v6, v7
	v_cvt_pk_bf16_f32 v7, v8, v9
	s_waitcnt lgkmcnt(0)
	v_mfma_f32_16x16x32_bf16 v[134:137], v[152:155], v[144:147], v[134:137]
	ds_read_b128 v[138:141], v157
	v_lshl_or_b32 v144, v156, 8, v204
	ds_read_b128 v[144:147], v144
	v_or_b32_e32 v156, 2, v143
	s_waitcnt lgkmcnt(1)
	v_mfma_f32_16x16x32_bf16 v[2:5], v[138:141], v[148:151], v[2:5]
	v_lshl_or_b32 v138, v156, 10, v198
	ds_read_b128 v[138:141], v138
	ds_read_b128 v[152:155], v221
	s_waitcnt lgkmcnt(2)
	v_mfma_f32_16x16x32_bf16 v[134:137], v[144:147], v[148:151], v[134:137]
	v_lshl_or_b32 v144, v156, 8, v204
	v_or_b32_e32 v156, 3, v143
	ds_read_b128 v[144:147], v144
	ds_read_b128 v[148:151], v219
	s_waitcnt lgkmcnt(2)
	v_mfma_f32_16x16x32_bf16 v[2:5], v[138:141], v[152:155], v[2:5]
	v_lshl_or_b32 v138, v156, 10, v198
	ds_read_b128 v[138:141], v138
	s_waitcnt lgkmcnt(2)
	v_mfma_f32_16x16x32_bf16 v[134:137], v[144:147], v[152:155], v[134:137]
	v_lshl_or_b32 v144, v156, 8, v204
	ds_read_b128 v[144:147], v144
	v_or_b32_e32 v152, 4, v143
	s_waitcnt lgkmcnt(1)
	v_mfma_f32_16x16x32_bf16 v[2:5], v[138:141], v[148:151], v[2:5]
	v_lshl_or_b32 v138, v152, 10, v198
	ds_read_b128 v[138:141], v138
	v_or_b32_e32 v156, 5, v143
	s_waitcnt lgkmcnt(1)
	v_mfma_f32_16x16x32_bf16 v[134:137], v[144:147], v[148:151], v[134:137]
	ds_read_b128 v[144:147], v218
	v_lshl_or_b32 v148, v152, 8, v204
	ds_read_b128 v[148:151], v148
	ds_read_b128 v[152:155], v217
	s_waitcnt lgkmcnt(2)
	v_mfma_f32_16x16x32_bf16 v[2:5], v[138:141], v[144:147], v[2:5]
	v_lshl_or_b32 v138, v156, 10, v198
	ds_read_b128 v[138:141], v138
	s_waitcnt lgkmcnt(2)
	v_mfma_f32_16x16x32_bf16 v[134:137], v[148:151], v[144:147], v[134:137]
	v_lshl_or_b32 v144, v156, 8, v204
	ds_read_b128 v[144:147], v144
	v_or_b32_e32 v148, 6, v143
	s_waitcnt lgkmcnt(1)
	v_mfma_f32_16x16x32_bf16 v[2:5], v[138:141], v[152:155], v[2:5]
	v_lshl_or_b32 v138, v148, 10, v198
	ds_read_b128 v[138:141], v138
	v_lshl_or_b32 v148, v148, 8, v204
	s_waitcnt lgkmcnt(1)
	v_mfma_f32_16x16x32_bf16 v[134:137], v[144:147], v[152:155], v[134:137]
	ds_read_b128 v[144:147], v216
	ds_read_b128 v[148:151], v148
	ds_read_b128 v[152:155], v213
	v_or_b32_e32 v143, 7, v143
	ds_write_b64 v212, v[6:7]
	s_waitcnt lgkmcnt(3)
	v_mfma_f32_16x16x32_bf16 v[2:5], v[138:141], v[144:147], v[2:5]
	v_lshl_or_b32 v138, v143, 10, v198
	v_lshl_or_b32 v143, v143, 8, v204
	s_waitcnt vmcnt(19)
	v_cvt_pk_bf16_f32 v6, v18, v19
	v_cvt_pk_bf16_f32 v7, v20, v21
	ds_read_b128 v[138:141], v138
	s_waitcnt lgkmcnt(3)
	v_mfma_f32_16x16x32_bf16 v[134:137], v[148:151], v[144:147], v[134:137]
	ds_read_b128 v[144:147], v143
	ds_write_b64 v211, v[6:7] offset:512
	s_waitcnt vmcnt(18)
	v_cvt_pk_bf16_f32 v6, v26, v27
	v_cvt_pk_bf16_f32 v7, v28, v29
	ds_write_b64 v210, v[6:7] offset:1024
	s_waitcnt vmcnt(17)
	v_cvt_pk_bf16_f32 v6, v34, v35
	v_cvt_pk_bf16_f32 v7, v36, v37
	ds_write_b64 v209, v[6:7] offset:1536
	s_waitcnt vmcnt(16)
	v_cvt_pk_bf16_f32 v6, v42, v43
	v_cvt_pk_bf16_f32 v7, v44, v45
	ds_write_b64 v208, v[6:7] offset:2048
	v_cvt_pk_bf16_f32 v6, v50, v51
	v_cvt_pk_bf16_f32 v7, v52, v53
	ds_write_b64 v207, v[6:7] offset:2560
	v_cvt_pk_bf16_f32 v6, v58, v59
	v_cvt_pk_bf16_f32 v7, v60, v61
	ds_write_b64 v206, v[6:7] offset:3072
	v_cvt_pk_bf16_f32 v6, v66, v67
	v_cvt_pk_bf16_f32 v7, v68, v69
	ds_write_b64 v205, v[6:7] offset:3584
	v_cvt_pk_bf16_f32 v6, v74, v75
	v_cvt_pk_bf16_f32 v7, v76, v77
	ds_write_b64 v231, v[6:7] offset:4096
	v_cvt_pk_bf16_f32 v6, v82, v83
	v_cvt_pk_bf16_f32 v7, v84, v85
	ds_write_b64 v230, v[6:7] offset:4608
	v_cvt_pk_bf16_f32 v6, v90, v91
	v_cvt_pk_bf16_f32 v7, v92, v93
	s_waitcnt lgkmcnt(9)
	v_mfma_f32_16x16x32_bf16 v[134:137], v[144:147], v[152:155], v[134:137]
	ds_write_b64 v229, v[6:7] offset:5120
	v_cvt_pk_bf16_f32 v6, v98, v99
	v_cvt_pk_bf16_f32 v7, v100, v101
	ds_write_b64 v228, v[6:7] offset:5632
	v_cvt_pk_bf16_f32 v6, v102, v103
	v_cvt_pk_bf16_f32 v7, v104, v105
	ds_write_b64 v227, v[6:7] offset:6144
	v_cvt_pk_bf16_f32 v6, v110, v111
	v_cvt_pk_bf16_f32 v7, v112, v113
	ds_write_b64 v226, v[6:7] offset:6656
	v_cvt_pk_bf16_f32 v6, v118, v119
	v_cvt_pk_bf16_f32 v7, v120, v121
	v_mfma_f32_16x16x32_bf16 v[2:5], v[138:141], v[152:155], v[2:5]
	ds_write_b64 v225, v[6:7] offset:7168
	v_cvt_pk_bf16_f32 v6, v126, v127
	v_cvt_pk_bf16_f32 v7, v128, v129
	ds_write_b64 v224, v[6:7] offset:7680
	v_add_u32_e32 v6, 48, v232
	v_and_b32_e32 v50, 56, v6
	v_lshl_or_b32 v6, v50, 10, v198
	v_lshl_or_b32 v34, v50, 8, v204
	ds_read_b128 v[6:9], v6
	ds_read_b128 v[18:21], v223
	ds_read_b128 v[26:29], v222
	ds_read_b128 v[34:37], v34
	v_or_b32_e32 v42, 1, v50
	v_lshl_or_b32 v43, v42, 10, v198
	s_waitcnt lgkmcnt(2)
	v_mfma_f32_16x16x32_bf16 v[2:5], v[6:9], v[18:21], v[2:5]
	ds_read_b128 v[6:9], v43
	v_or_b32_e32 v51, 2, v50
	s_waitcnt lgkmcnt(1)
	v_mfma_f32_16x16x32_bf16 v[18:21], v[34:37], v[18:21], v[134:137]
	v_lshl_or_b32 v34, v42, 8, v204
	ds_read_b128 v[34:37], v34
	s_waitcnt lgkmcnt(1)
	v_mfma_f32_16x16x32_bf16 v[2:5], v[6:9], v[26:29], v[2:5]
	v_lshl_or_b32 v6, v51, 10, v198
	ds_read_b128 v[6:9], v6
	ds_read_b128 v[42:45], v221
	s_waitcnt lgkmcnt(2)
	v_mfma_f32_16x16x32_bf16 v[18:21], v[34:37], v[26:29], v[18:21]
	v_lshl_or_b32 v26, v51, 8, v204
	v_or_b32_e32 v51, 3, v50
	ds_read_b128 v[26:29], v26
	ds_read_b128 v[34:37], v219
	s_waitcnt lgkmcnt(2)
	v_mfma_f32_16x16x32_bf16 v[2:5], v[6:9], v[42:45], v[2:5]
	v_lshl_or_b32 v6, v51, 10, v198
	ds_read_b128 v[6:9], v6
	s_waitcnt lgkmcnt(2)
	v_mfma_f32_16x16x32_bf16 v[18:21], v[26:29], v[42:45], v[18:21]
	v_lshl_or_b32 v26, v51, 8, v204
	ds_read_b128 v[26:29], v26
	v_or_b32_e32 v42, 4, v50
	s_waitcnt lgkmcnt(1)
	v_mfma_f32_16x16x32_bf16 v[2:5], v[6:9], v[34:37], v[2:5]
	v_lshl_or_b32 v6, v42, 10, v198
	ds_read_b128 v[6:9], v6
	v_or_b32_e32 v51, 5, v50
	s_waitcnt lgkmcnt(1)
	v_mfma_f32_16x16x32_bf16 v[18:21], v[26:29], v[34:37], v[18:21]
	ds_read_b128 v[26:29], v218
	v_lshl_or_b32 v34, v42, 8, v204
	ds_read_b128 v[34:37], v34
	ds_read_b128 v[42:45], v217
	s_waitcnt lgkmcnt(2)
	v_mfma_f32_16x16x32_bf16 v[2:5], v[6:9], v[26:29], v[2:5]
	v_lshl_or_b32 v6, v51, 10, v198
	ds_read_b128 v[6:9], v6
	s_waitcnt lgkmcnt(2)
	v_mfma_f32_16x16x32_bf16 v[18:21], v[34:37], v[26:29], v[18:21]
	v_lshl_or_b32 v26, v51, 8, v204
	ds_read_b128 v[26:29], v26
	v_or_b32_e32 v34, 6, v50
	s_waitcnt lgkmcnt(1)
	v_mfma_f32_16x16x32_bf16 v[2:5], v[6:9], v[42:45], v[2:5]
	v_lshl_or_b32 v6, v34, 10, v198
	ds_read_b128 v[6:9], v6
	v_lshl_or_b32 v34, v34, 8, v204
	s_waitcnt lgkmcnt(1)
	v_mfma_f32_16x16x32_bf16 v[18:21], v[26:29], v[42:45], v[18:21]
	ds_read_b128 v[26:29], v216
	ds_read_b128 v[34:37], v34
	ds_read_b128 v[42:45], v213
	v_or_b32_e32 v50, 7, v50
	s_waitcnt lgkmcnt(2)
	v_mfma_f32_16x16x32_bf16 v[2:5], v[6:9], v[26:29], v[2:5]
	v_lshl_or_b32 v6, v50, 10, v198
	ds_read_b128 v[6:9], v6
	s_waitcnt lgkmcnt(2)
	v_mfma_f32_16x16x32_bf16 v[18:21], v[34:37], v[26:29], v[18:21]
	v_lshl_or_b32 v26, v50, 8, v204
	ds_read_b128 v[26:29], v26
	s_waitcnt lgkmcnt(1)
	v_mfma_f32_16x16x32_bf16 v[34:37], v[6:9], v[42:45], v[2:5]
	v_and_b32_e32 v74, 7, v197
	v_lshrrev_b32_e32 v75, 3, v197
	v_lshlrev_b32_e32 v192, 13, v200
	v_lshlrev_b32_e32 v193, 11, v200
	v_lshl_add_u32 v203, v197, 2, v196
	v_lshl_or_b32 v192, v75, 8, v192
	v_lshl_or_b32 v193, v75, 6, v193
	v_add_u32_e32 v203, 0x24800, v203
	v_lshl_or_b32 v192, v201, 6, v192
	v_lshl_or_b32 v193, v74, 1, v193
	v_lshl_or_b32 v192, v74, 1, v192
	v_or_b32_e32 v193, 0x10000, v193
	v_cmp_gt_u32_e64 s[36:37], 16, v1
	v_cmp_eq_u32_e64 s[38:39], 1, v201
	ds_read2_b32 v[2:3], v203 offset1:16
	ds_read2_b32 v[4:5], v203 offset0:32 offset1:48
	ds_read2_b32 v[6:7], v203 offset0:64 offset1:80
	ds_read2_b32 v[8:9], v203 offset0:96 offset1:112
	ds_read2_b32 v[50:51], v203 offset0:128 offset1:144
	ds_read2_b32 v[52:53], v203 offset0:160 offset1:176
	ds_read2_b32 v[58:59], v203 offset0:192 offset1:208
	ds_read2_b32 v[60:61], v203 offset0:224 offset1:240
	v_mov_b32_e32 v146, 0
	v_mov_b32_e32 v147, 0
	v_mov_b32_e32 v150, 0
	v_mov_b32_e32 v151, 0
	v_mov_b32_e32 v154, 0
	v_mov_b32_e32 v155, 0
	v_mov_b32_e32 v158, 0
	v_mov_b32_e32 v159, 0
	v_mov_b32_e32 v162, 0
	v_mov_b32_e32 v163, 0
	v_mov_b32_e32 v166, 0
	v_mov_b32_e32 v167, 0
	v_mov_b32_e32 v170, 0
	v_mov_b32_e32 v171, 0
	v_mov_b32_e32 v174, 0
	v_mov_b32_e32 v175, 0
	v_mov_b32_e32 v178, 0
	v_mov_b32_e32 v179, 0
	v_mov_b32_e32 v182, 0
	v_mov_b32_e32 v183, 0
	v_mov_b32_e32 v186, 0
	v_mov_b32_e32 v187, 0
	v_mov_b32_e32 v190, 0
	v_mov_b32_e32 v191, 0
	v_mov_b32_e32 v234, 0
	v_mov_b32_e32 v235, 0
	v_mov_b32_e32 v238, 0
	v_mov_b32_e32 v239, 0
	v_mov_b32_e32 v242, 0
	v_mov_b32_e32 v243, 0
	v_mov_b32_e32 v246, 0
	v_mov_b32_e32 v247, 0
	ds_read_u16 v82, v192
	ds_read_u16 v83, v192 offset:16
	ds_read_u16 v84, v192 offset:32
	ds_read_u16 v85, v192 offset:48
	ds_read_u16 v90, v193
	ds_read_u16 v91, v193 offset:16
	ds_read_u16 v92, v193 offset:32
	ds_read_u16 v93, v193 offset:48
	ds_read_u16 v98, v192 offset:512
	ds_read_u16 v99, v192 offset:528
	ds_read_u16 v100, v192 offset:544
	ds_read_u16 v101, v192 offset:560
	ds_read_u16 v102, v193 offset:128
	ds_read_u16 v103, v193 offset:144
	ds_read_u16 v104, v193 offset:160
	ds_read_u16 v105, v193 offset:176
	s_waitcnt lgkmcnt(8)
	v_lshl_or_b32 v144, v83, 16, v82
	v_lshl_or_b32 v145, v85, 16, v84
	s_mov_b64 exec, s[36:37]
	v_lshl_or_b32 v146, v91, 16, v90
	v_lshl_or_b32 v147, v93, 16, v92
	s_mov_b64 exec, -1
	ds_read_u16 v82, v192 offset:1024
	ds_read_u16 v83, v192 offset:1040
	ds_read_u16 v84, v192 offset:1056
	ds_read_u16 v85, v192 offset:1072
	ds_read_u16 v90, v193 offset:256
	ds_read_u16 v91, v193 offset:272
	ds_read_u16 v92, v193 offset:288
	ds_read_u16 v93, v193 offset:304
	s_waitcnt lgkmcnt(8)
	v_lshl_or_b32 v148, v99, 16, v98
	v_lshl_or_b32 v149, v101, 16, v100
	s_mov_b64 exec, s[36:37]
	v_lshl_or_b32 v150, v103, 16, v102
	v_lshl_or_b32 v151, v105, 16, v104
	s_mov_b64 exec, -1
	ds_read_u16 v98, v192 offset:1536
	ds_read_u16 v99, v192 offset:1552
	ds_read_u16 v100, v192 offset:1568
	ds_read_u16 v101, v192 offset:1584
	ds_read_u16 v102, v193 offset:384
	ds_read_u16 v103, v193 offset:400
	ds_read_u16 v104, v193 offset:416
	ds_read_u16 v105, v193 offset:432
	s_waitcnt lgkmcnt(8)
	v_lshl_or_b32 v152, v83, 16, v82
	v_lshl_or_b32 v153, v85, 16, v84
	s_mov_b64 exec, s[36:37]
	v_lshl_or_b32 v154, v91, 16, v90
	v_lshl_or_b32 v155, v93, 16, v92
	s_mov_b64 exec, -1
	ds_read_u16 v82, v192 offset:2048
	ds_read_u16 v83, v192 offset:2064
	ds_read_u16 v84, v192 offset:2080
	ds_read_u16 v85, v192 offset:2096
	ds_read_u16 v90, v193 offset:512
	ds_read_u16 v91, v193 offset:528
	ds_read_u16 v92, v193 offset:544
	ds_read_u16 v93, v193 offset:560
	s_waitcnt lgkmcnt(8)
	v_lshl_or_b32 v156, v99, 16, v98
	v_lshl_or_b32 v157, v101, 16, v100
	s_mov_b64 exec, s[36:37]
	v_lshl_or_b32 v158, v103, 16, v102
	v_lshl_or_b32 v159, v105, 16, v104
	s_mov_b64 exec, -1
	ds_read_u16 v98, v192 offset:2560
	ds_read_u16 v99, v192 offset:2576
	ds_read_u16 v100, v192 offset:2592
	ds_read_u16 v101, v192 offset:2608
	ds_read_u16 v102, v193 offset:640
	ds_read_u16 v103, v193 offset:656
	ds_read_u16 v104, v193 offset:672
	ds_read_u16 v105, v193 offset:688
	s_waitcnt lgkmcnt(8)
	v_lshl_or_b32 v160, v83, 16, v82
	v_lshl_or_b32 v161, v85, 16, v84
	s_mov_b64 exec, s[36:37]
	v_lshl_or_b32 v162, v91, 16, v90
	v_lshl_or_b32 v163, v93, 16, v92
	s_mov_b64 exec, -1
	ds_read_u16 v82, v192 offset:3072
	ds_read_u16 v83, v192 offset:3088
	ds_read_u16 v84, v192 offset:3104
	ds_read_u16 v85, v192 offset:3120
	ds_read_u16 v90, v193 offset:768
	ds_read_u16 v91, v193 offset:784
	ds_read_u16 v92, v193 offset:800
	ds_read_u16 v93, v193 offset:816
	s_waitcnt lgkmcnt(8)
	v_lshl_or_b32 v164, v99, 16, v98
	v_lshl_or_b32 v165, v101, 16, v100
	s_mov_b64 exec, s[36:37]
	v_lshl_or_b32 v166, v103, 16, v102
	v_lshl_or_b32 v167, v105, 16, v104
	s_mov_b64 exec, -1
	ds_read_u16 v98, v192 offset:3584
	ds_read_u16 v99, v192 offset:3600
	ds_read_u16 v100, v192 offset:3616
	ds_read_u16 v101, v192 offset:3632
	ds_read_u16 v102, v193 offset:896
	ds_read_u16 v103, v193 offset:912
	ds_read_u16 v104, v193 offset:928
	ds_read_u16 v105, v193 offset:944
	s_waitcnt lgkmcnt(8)
	v_lshl_or_b32 v168, v83, 16, v82
	v_lshl_or_b32 v169, v85, 16, v84
	s_mov_b64 exec, s[36:37]
	v_lshl_or_b32 v170, v91, 16, v90
	v_lshl_or_b32 v171, v93, 16, v92
	s_mov_b64 exec, -1
	ds_read_u16 v82, v192 offset:4096
	ds_read_u16 v83, v192 offset:4112
	ds_read_u16 v84, v192 offset:4128
	ds_read_u16 v85, v192 offset:4144
	ds_read_u16 v90, v193 offset:1024
	ds_read_u16 v91, v193 offset:1040
	ds_read_u16 v92, v193 offset:1056
	ds_read_u16 v93, v193 offset:1072
	s_waitcnt lgkmcnt(8)
	v_lshl_or_b32 v172, v99, 16, v98
	v_lshl_or_b32 v173, v101, 16, v100
	s_mov_b64 exec, s[36:37]
	v_lshl_or_b32 v174, v103, 16, v102
	v_lshl_or_b32 v175, v105, 16, v104
	s_mov_b64 exec, -1
	ds_read_u16 v98, v192 offset:4608
	ds_read_u16 v99, v192 offset:4624
	ds_read_u16 v100, v192 offset:4640
	ds_read_u16 v101, v192 offset:4656
	ds_read_u16 v102, v193 offset:1152
	ds_read_u16 v103, v193 offset:1168
	ds_read_u16 v104, v193 offset:1184
	ds_read_u16 v105, v193 offset:1200
	s_waitcnt lgkmcnt(8)
	v_lshl_or_b32 v176, v83, 16, v82
	v_lshl_or_b32 v177, v85, 16, v84
	s_mov_b64 exec, s[36:37]
	v_lshl_or_b32 v178, v91, 16, v90
	v_lshl_or_b32 v179, v93, 16, v92
	s_mov_b64 exec, -1
	ds_read_u16 v82, v192 offset:5120
	ds_read_u16 v83, v192 offset:5136
	ds_read_u16 v84, v192 offset:5152
	ds_read_u16 v85, v192 offset:5168
	ds_read_u16 v90, v193 offset:1280
	ds_read_u16 v91, v193 offset:1296
	ds_read_u16 v92, v193 offset:1312
	ds_read_u16 v93, v193 offset:1328
	s_waitcnt lgkmcnt(8)
	v_lshl_or_b32 v180, v99, 16, v98
	v_lshl_or_b32 v181, v101, 16, v100
	s_mov_b64 exec, s[36:37]
	v_lshl_or_b32 v182, v103, 16, v102
	v_lshl_or_b32 v183, v105, 16, v104
	s_mov_b64 exec, -1
	ds_read_u16 v98, v192 offset:5632
	ds_read_u16 v99, v192 offset:5648
	ds_read_u16 v100, v192 offset:5664
	ds_read_u16 v101, v192 offset:5680
	ds_read_u16 v102, v193 offset:1408
	ds_read_u16 v103, v193 offset:1424
	ds_read_u16 v104, v193 offset:1440
	ds_read_u16 v105, v193 offset:1456
	s_waitcnt lgkmcnt(8)
	v_lshl_or_b32 v184, v83, 16, v82
	v_lshl_or_b32 v185, v85, 16, v84
	s_mov_b64 exec, s[36:37]
	v_lshl_or_b32 v186, v91, 16, v90
	v_lshl_or_b32 v187, v93, 16, v92
	s_mov_b64 exec, -1
	ds_read_u16 v82, v192 offset:6144
	ds_read_u16 v83, v192 offset:6160
	ds_read_u16 v84, v192 offset:6176
	ds_read_u16 v85, v192 offset:6192
	ds_read_u16 v90, v193 offset:1536
	ds_read_u16 v91, v193 offset:1552
	ds_read_u16 v92, v193 offset:1568
	ds_read_u16 v93, v193 offset:1584
	s_waitcnt lgkmcnt(8)
	v_lshl_or_b32 v188, v99, 16, v98
	v_lshl_or_b32 v189, v101, 16, v100
	s_mov_b64 exec, s[36:37]
	v_lshl_or_b32 v190, v103, 16, v102
	v_lshl_or_b32 v191, v105, 16, v104
	s_mov_b64 exec, -1
	ds_read_u16 v98, v192 offset:6656
	ds_read_u16 v99, v192 offset:6672
	ds_read_u16 v100, v192 offset:6688
	ds_read_u16 v101, v192 offset:6704
	ds_read_u16 v102, v193 offset:1664
	ds_read_u16 v103, v193 offset:1680
	ds_read_u16 v104, v193 offset:1696
	ds_read_u16 v105, v193 offset:1712
	s_waitcnt lgkmcnt(8)
	v_lshl_or_b32 v232, v83, 16, v82
	v_lshl_or_b32 v233, v85, 16, v84
	s_mov_b64 exec, s[36:37]
	v_lshl_or_b32 v234, v91, 16, v90
	v_lshl_or_b32 v235, v93, 16, v92
	s_mov_b64 exec, -1
	ds_read_u16 v82, v192 offset:7168
	ds_read_u16 v83, v192 offset:7184
	ds_read_u16 v84, v192 offset:7200
	ds_read_u16 v85, v192 offset:7216
	ds_read_u16 v90, v193 offset:1792
	ds_read_u16 v91, v193 offset:1808
	ds_read_u16 v92, v193 offset:1824
	ds_read_u16 v93, v193 offset:1840
	s_waitcnt lgkmcnt(8)
	v_lshl_or_b32 v236, v99, 16, v98
	v_lshl_or_b32 v237, v101, 16, v100
	s_mov_b64 exec, s[36:37]
	v_lshl_or_b32 v238, v103, 16, v102
	v_lshl_or_b32 v239, v105, 16, v104
	s_mov_b64 exec, -1
	ds_read_u16 v98, v192 offset:7680
	ds_read_u16 v99, v192 offset:7696
	ds_read_u16 v100, v192 offset:7712
	ds_read_u16 v101, v192 offset:7728
	ds_read_u16 v102, v193 offset:1920
	ds_read_u16 v103, v193 offset:1936
	ds_read_u16 v104, v193 offset:1952
	ds_read_u16 v105, v193 offset:1968
	s_waitcnt lgkmcnt(8)
	v_lshl_or_b32 v240, v83, 16, v82
	v_lshl_or_b32 v241, v85, 16, v84
	s_mov_b64 exec, s[36:37]
	v_lshl_or_b32 v242, v91, 16, v90
	v_lshl_or_b32 v243, v93, 16, v92
	s_mov_b64 exec, -1
	s_waitcnt lgkmcnt(0)
	v_lshl_or_b32 v244, v99, 16, v98
	v_lshl_or_b32 v245, v101, 16, v100
	s_mov_b64 exec, s[36:37]
	v_lshl_or_b32 v246, v103, 16, v102
	v_lshl_or_b32 v247, v105, 16, v104
	s_mov_b64 exec, -1
	s_waitcnt lgkmcnt(0)
	s_mov_b64 exec, s[38:39]
	v_cvt_pk_bf16_f32 v66, v2, v195
	v_cvt_pk_bf16_f32 v74, v3, v195
	v_lshlrev_b32_e32 v67, 16, v66
	v_lshlrev_b32_e32 v75, 16, v74
	v_sub_f32_e32 v2, v2, v67
	v_sub_f32_e32 v3, v3, v75
	v_cvt_pk_bf16_f32 v68, v2, v195
	v_cvt_pk_bf16_f32 v76, v3, v195
	v_lshlrev_b32_e32 v69, 16, v68
	v_lshlrev_b32_e32 v77, 16, v76
	v_sub_f32_e32 v2, v2, v69
	v_sub_f32_e32 v3, v3, v77
	v_cvt_pk_bf16_f32 v147, v2, v195
	v_cvt_pk_bf16_f32 v151, v3, v195
	v_cvt_pk_bf16_f32 v146, v67, v69
	v_cvt_pk_bf16_f32 v150, v75, v77
	v_cvt_pk_bf16_f32 v66, v4, v195
	v_cvt_pk_bf16_f32 v74, v5, v195
	v_lshlrev_b32_e32 v67, 16, v66
	v_lshlrev_b32_e32 v75, 16, v74
	v_sub_f32_e32 v4, v4, v67
	v_sub_f32_e32 v5, v5, v75
	v_cvt_pk_bf16_f32 v68, v4, v195
	v_cvt_pk_bf16_f32 v76, v5, v195
	v_lshlrev_b32_e32 v69, 16, v68
	v_lshlrev_b32_e32 v77, 16, v76
	v_sub_f32_e32 v4, v4, v69
	v_sub_f32_e32 v5, v5, v77
	v_cvt_pk_bf16_f32 v155, v4, v195
	v_cvt_pk_bf16_f32 v159, v5, v195
	v_cvt_pk_bf16_f32 v154, v67, v69
	v_cvt_pk_bf16_f32 v158, v75, v77
	v_cvt_pk_bf16_f32 v66, v6, v195
	v_cvt_pk_bf16_f32 v74, v7, v195
	v_lshlrev_b32_e32 v67, 16, v66
	v_lshlrev_b32_e32 v75, 16, v74
	v_sub_f32_e32 v6, v6, v67
	v_sub_f32_e32 v7, v7, v75
	v_cvt_pk_bf16_f32 v68, v6, v195
	v_cvt_pk_bf16_f32 v76, v7, v195
	v_lshlrev_b32_e32 v69, 16, v68
	v_lshlrev_b32_e32 v77, 16, v76
	v_sub_f32_e32 v6, v6, v69
	v_sub_f32_e32 v7, v7, v77
	v_cvt_pk_bf16_f32 v163, v6, v195
	v_cvt_pk_bf16_f32 v167, v7, v195
	v_cvt_pk_bf16_f32 v162, v67, v69
	v_cvt_pk_bf16_f32 v166, v75, v77
	v_cvt_pk_bf16_f32 v66, v8, v195
	v_cvt_pk_bf16_f32 v74, v9, v195
	v_lshlrev_b32_e32 v67, 16, v66
	v_lshlrev_b32_e32 v75, 16, v74
	v_sub_f32_e32 v8, v8, v67
	v_sub_f32_e32 v9, v9, v75
	v_cvt_pk_bf16_f32 v68, v8, v195
	v_cvt_pk_bf16_f32 v76, v9, v195
	v_lshlrev_b32_e32 v69, 16, v68
	v_lshlrev_b32_e32 v77, 16, v76
	v_sub_f32_e32 v8, v8, v69
	v_sub_f32_e32 v9, v9, v77
	v_cvt_pk_bf16_f32 v171, v8, v195
	v_cvt_pk_bf16_f32 v175, v9, v195
	v_cvt_pk_bf16_f32 v170, v67, v69
	v_cvt_pk_bf16_f32 v174, v75, v77
	v_cvt_pk_bf16_f32 v66, v50, v195
	v_cvt_pk_bf16_f32 v74, v51, v195
	v_lshlrev_b32_e32 v67, 16, v66
	v_lshlrev_b32_e32 v75, 16, v74
	v_sub_f32_e32 v50, v50, v67
	v_sub_f32_e32 v51, v51, v75
	v_cvt_pk_bf16_f32 v68, v50, v195
	v_cvt_pk_bf16_f32 v76, v51, v195
	v_lshlrev_b32_e32 v69, 16, v68
	v_lshlrev_b32_e32 v77, 16, v76
	v_sub_f32_e32 v50, v50, v69
	v_sub_f32_e32 v51, v51, v77
	v_cvt_pk_bf16_f32 v179, v50, v195
	v_cvt_pk_bf16_f32 v183, v51, v195
	v_cvt_pk_bf16_f32 v178, v67, v69
	v_cvt_pk_bf16_f32 v182, v75, v77
	v_cvt_pk_bf16_f32 v66, v52, v195
	v_cvt_pk_bf16_f32 v74, v53, v195
	v_lshlrev_b32_e32 v67, 16, v66
	v_lshlrev_b32_e32 v75, 16, v74
	v_sub_f32_e32 v52, v52, v67
	v_sub_f32_e32 v53, v53, v75
	v_cvt_pk_bf16_f32 v68, v52, v195
	v_cvt_pk_bf16_f32 v76, v53, v195
	v_lshlrev_b32_e32 v69, 16, v68
	v_lshlrev_b32_e32 v77, 16, v76
	v_sub_f32_e32 v52, v52, v69
	v_sub_f32_e32 v53, v53, v77
	v_cvt_pk_bf16_f32 v187, v52, v195
	v_cvt_pk_bf16_f32 v191, v53, v195
	v_cvt_pk_bf16_f32 v186, v67, v69
	v_cvt_pk_bf16_f32 v190, v75, v77
	v_cvt_pk_bf16_f32 v66, v58, v195
	v_cvt_pk_bf16_f32 v74, v59, v195
	v_lshlrev_b32_e32 v67, 16, v66
	v_lshlrev_b32_e32 v75, 16, v74
	v_sub_f32_e32 v58, v58, v67
	v_sub_f32_e32 v59, v59, v75
	v_cvt_pk_bf16_f32 v68, v58, v195
	v_cvt_pk_bf16_f32 v76, v59, v195
	v_lshlrev_b32_e32 v69, 16, v68
	v_lshlrev_b32_e32 v77, 16, v76
	v_sub_f32_e32 v58, v58, v69
	v_sub_f32_e32 v59, v59, v77
	v_cvt_pk_bf16_f32 v235, v58, v195
	v_cvt_pk_bf16_f32 v239, v59, v195
	v_cvt_pk_bf16_f32 v234, v67, v69
	v_cvt_pk_bf16_f32 v238, v75, v77
	v_cvt_pk_bf16_f32 v66, v60, v195
	v_cvt_pk_bf16_f32 v74, v61, v195
	v_lshlrev_b32_e32 v67, 16, v66
	v_lshlrev_b32_e32 v75, 16, v74
	v_sub_f32_e32 v60, v60, v67
	v_sub_f32_e32 v61, v61, v75
	v_cvt_pk_bf16_f32 v68, v60, v195
	v_cvt_pk_bf16_f32 v76, v61, v195
	v_lshlrev_b32_e32 v69, 16, v68
	v_lshlrev_b32_e32 v77, 16, v76
	v_sub_f32_e32 v60, v60, v69
	v_sub_f32_e32 v61, v61, v77
	v_cvt_pk_bf16_f32 v243, v60, v195
	v_cvt_pk_bf16_f32 v247, v61, v195
	v_cvt_pk_bf16_f32 v242, v67, v69
	v_cvt_pk_bf16_f32 v246, v75, v77
	s_mov_b64 exec, -1
	s_waitcnt vmcnt(15)
	v_cvt_pk_bf16_f32 v6, v10, v11
	v_cvt_pk_bf16_f32 v7, v12, v13
	ds_write_b64 v212, v[6:7]
	s_waitcnt vmcnt(14)
	v_cvt_pk_bf16_f32 v6, v14, v15
	v_cvt_pk_bf16_f32 v7, v16, v17
	ds_write_b64 v211, v[6:7] offset:512
	s_waitcnt vmcnt(13)
	v_cvt_pk_bf16_f32 v6, v22, v23
	v_cvt_pk_bf16_f32 v7, v24, v25
	ds_write_b64 v210, v[6:7] offset:1024
	s_waitcnt vmcnt(12)
	v_cvt_pk_bf16_f32 v6, v30, v31
	v_cvt_pk_bf16_f32 v7, v32, v33
	ds_write_b64 v209, v[6:7] offset:1536
	s_waitcnt vmcnt(11)
	v_cvt_pk_bf16_f32 v6, v38, v39
	v_cvt_pk_bf16_f32 v7, v40, v41
	ds_write_b64 v208, v[6:7] offset:2048
	s_waitcnt vmcnt(10)
	v_cvt_pk_bf16_f32 v6, v46, v47
	v_cvt_pk_bf16_f32 v7, v48, v49
	ds_write_b64 v207, v[6:7] offset:2560
	s_waitcnt vmcnt(9)
	v_cvt_pk_bf16_f32 v6, v54, v55
	v_cvt_pk_bf16_f32 v7, v56, v57
	ds_write_b64 v206, v[6:7] offset:3072
	s_waitcnt vmcnt(8)
	v_cvt_pk_bf16_f32 v6, v62, v63
	v_cvt_pk_bf16_f32 v7, v64, v65
	ds_write_b64 v205, v[6:7] offset:3584
	s_waitcnt vmcnt(7)
	v_cvt_pk_bf16_f32 v6, v70, v71
	v_cvt_pk_bf16_f32 v7, v72, v73
	ds_write_b64 v231, v[6:7] offset:4096
	s_waitcnt vmcnt(6)
	v_cvt_pk_bf16_f32 v6, v78, v79
	v_cvt_pk_bf16_f32 v7, v80, v81
	ds_write_b64 v230, v[6:7] offset:4608
	s_waitcnt vmcnt(5)
	v_cvt_pk_bf16_f32 v6, v86, v87
	v_cvt_pk_bf16_f32 v7, v88, v89
	ds_write_b64 v229, v[6:7] offset:5120
	s_waitcnt vmcnt(4)
	v_cvt_pk_bf16_f32 v6, v94, v95
	v_cvt_pk_bf16_f32 v7, v96, v97
	ds_write_b64 v228, v[6:7] offset:5632
	s_waitcnt vmcnt(3)
	v_cvt_pk_bf16_f32 v6, v106, v107
	v_cvt_pk_bf16_f32 v7, v108, v109
	ds_write_b64 v227, v[6:7] offset:6144
	s_waitcnt vmcnt(2)
	v_cvt_pk_bf16_f32 v6, v114, v115
	v_cvt_pk_bf16_f32 v7, v116, v117
	ds_write_b64 v226, v[6:7] offset:6656
	s_waitcnt vmcnt(1)
	v_cvt_pk_bf16_f32 v6, v122, v123
	v_cvt_pk_bf16_f32 v7, v124, v125
	s_waitcnt lgkmcnt(14)
	v_mfma_f32_16x16x32_bf16 v[2:5], v[26:29], v[42:45], v[18:21]
	ds_write_b64 v225, v[6:7] offset:7168
	s_waitcnt vmcnt(0)
	v_cvt_pk_bf16_f32 v6, v130, v131
	v_cvt_pk_bf16_f32 v7, v132, v133
	ds_write_b64 v224, v[6:7] offset:7680
	v_lshlrev_b32_e32 v6, 3, v142
	v_and_b32_e32 v58, 56, v6
	v_lshl_or_b32 v6, v58, 10, v198
	v_or_b32_e32 v18, 1, v58
	v_lshl_or_b32 v7, v58, 8, v204
	ds_read_b128 v[14:17], v6
	ds_read_b128 v[10:13], v7
	v_lshl_or_b32 v6, v18, 10, v198
	ds_read_b128 v[26:29], v6
	ds_read_b128 v[22:25], v223
	ds_read_b128 v[6:9], v222
	v_or_b32_e32 v42, 2, v58
	v_lshl_or_b32 v19, v42, 10, v198
	ds_read_b128 v[38:41], v19
	s_waitcnt lgkmcnt(2)
	v_mfma_f32_16x16x32_bf16 v[30:33], v[14:17], v[22:25], v[34:37]
	v_lshl_or_b32 v14, v18, 8, v204
	ds_read_b128 v[18:21], v14
	ds_read_b128 v[14:17], v221
	v_or_b32_e32 v59, 5, v58
	s_waitcnt lgkmcnt(3)
	v_mfma_f32_16x16x32_bf16 v[34:37], v[26:29], v[6:9], v[30:33]
	v_lshl_or_b32 v26, v42, 8, v204
	ds_read_b128 v[26:29], v26
	s_nop 0
	ds_read_b128 v[30:33], v219
	v_or_b32_e32 v68, 6, v58
	s_waitcnt lgkmcnt(2)
	v_mfma_f32_16x16x32_bf16 v[38:41], v[38:41], v[14:17], v[34:37]
	v_lshl_or_b32 v64, v68, 10, v198
	s_nop 1
	v_or_b32_e32 v34, 3, v58
	v_lshl_or_b32 v35, v34, 10, v198
	ds_read_b128 v[42:45], v35
	v_lshl_or_b32 v34, v34, 8, v204
	s_waitcnt lgkmcnt(0)
	v_mfma_f32_16x16x32_bf16 v[46:49], v[42:45], v[30:33], v[38:41]
	s_nop 2
	v_or_b32_e32 v38, 4, v58
	v_lshl_or_b32 v39, v38, 10, v198
	v_lshl_or_b32 v38, v38, 8, v204
	ds_read_b128 v[34:37], v34
	ds_read_b128 v[50:53], v39
	ds_read_b128 v[42:45], v38
	v_lshl_or_b32 v38, v59, 10, v198
	ds_read_b128 v[54:57], v38
	ds_read_b128 v[60:63], v218
	ds_read_b128 v[38:41], v217
	ds_read_b128 v[72:75], v64
	s_waitcnt lgkmcnt(2)
	v_mfma_f32_16x16x32_bf16 v[64:67], v[50:53], v[60:63], v[46:49]
	v_or_b32_e32 v58, 7, v58
	s_nop 1
	v_lshl_or_b32 v46, v59, 8, v204
	v_lshl_or_b32 v59, v68, 8, v204
	ds_read_b128 v[50:53], v46
	ds_read_b128 v[46:49], v216
	s_waitcnt lgkmcnt(3)
	v_mfma_f32_16x16x32_bf16 v[54:57], v[54:57], v[38:41], v[64:67]
	s_nop 2
	ds_read_b128 v[64:67], v59
	ds_read_b128 v[68:71], v213
	v_lshl_or_b32 v59, v58, 10, v198
	ds_read_b128 v[76:79], v59
	s_waitcnt lgkmcnt(3)
	v_mfma_f32_16x16x32_bf16 v[54:57], v[72:75], v[46:49], v[54:57]
	v_lshl_or_b32 v58, v58, 8, v204
	ds_read_b128 v[72:75], v58
	s_waitcnt lgkmcnt(1)
	v_mfma_f32_16x16x32_bf16 v[56:59], v[76:79], v[68:71], v[54:57]
	s_nop 2
	v_add_u32_e32 v76, 0x24800, v196
	s_waitcnt lgkmcnt(0)
	v_mfma_f32_16x16x32_bf16 v[2:5], v[10:13], v[22:25], v[2:5]
	v_mfma_f32_16x16x32_bf16 v[2:5], v[18:21], v[6:9], v[2:5]
	s_waitcnt lgkmcnt(0)
	v_mfma_f32_16x16x32_bf16 v[2:5], v[26:29], v[14:17], v[2:5]
	v_mfma_f32_16x16x32_bf16 v[2:5], v[34:37], v[30:33], v[2:5]
	s_waitcnt lgkmcnt(0)
	v_mfma_f32_16x16x32_bf16 v[2:5], v[42:45], v[60:63], v[2:5]
	v_mfma_f32_16x16x32_bf16 v[2:5], v[50:53], v[38:41], v[2:5]
	s_waitcnt lgkmcnt(0)
	v_mfma_f32_16x16x32_bf16 v[2:5], v[64:67], v[46:49], v[2:5]
	v_mfma_f32_16x16x32_bf16 v[60:63], v[72:75], v[68:71], v[2:5]
	s_waitcnt lgkmcnt(0)
	v_cmp_gt_u32_e64 s[0:1], 16, v1
	v_cmp_lt_u32_e32 vcc, 15, v1
	s_waitcnt lgkmcnt(0)
	s_nop 2
	v_max_f32_e32 v2, v59, v59
	v_max_f32_e32 v3, v58, v58
	s_waitcnt lgkmcnt(0)
	v_max_f32_e32 v2, v3, v2
	s_nop 0
	s_nop 0
	s_nop 0
	s_waitcnt lgkmcnt(0)
	s_nop 0
	s_nop 0
	s_and_saveexec_b64 s[4:5], vcc
	s_xor_b64 s[4:5], exec, s[4:5]
	s_or_saveexec_b64 s[4:5], s[4:5]
	v_max3_f32 v53, v56, v57, v2
	s_xor_b64 exec, exec, s[4:5]
	v_max_f32_e32 v2, v61, v61
	v_max_f32_e32 v3, v60, v60
	v_max_f32_e32 v2, v3, v2
	v_max_f32_e32 v3, v63, v63
	v_max_f32_e32 v4, v62, v62
	v_max_f32_e32 v3, v4, v3
	v_max3_f32 v53, v53, v2, v3
	s_or_b64 exec, exec, s[4:5]
	v_cmp_eq_u32_e64 s[4:5], 1, v201
	v_max_f32_e32 v53, v53, v53
	v_mov_b32_e32 v68, v53
	s_nop 1
	v_permlane16_swap_b32_e32 v53, v68
	v_max_f32_e32 v68, v53, v68
	v_mov_b32_e32 v55, v68
	s_nop 1
	v_permlane32_swap_b32_e32 v68, v55
	v_max_f32_e32 v68, v68, v55
	v_sub_f32_e32 v55, v56, v68
	v_mul_f32_e32 v55, 0x3fb8aa3b, v55
	v_exp_f32_e32 v70, v55
	v_sub_f32_e32 v55, v57, v68
	v_sub_f32_e32 v57, v59, v68
	v_mul_f32_e32 v57, 0x3fb8aa3b, v57
	v_mul_f32_e32 v55, 0x3fb8aa3b, v55
	v_exp_f32_e32 v59, v57
	v_sub_f32_e32 v57, v60, v68
	v_exp_f32_e32 v71, v55
	v_sub_f32_e32 v55, v58, v68
	v_mul_f32_e32 v57, 0x3fb8aa3b, v57
	v_sub_f32_e32 v58, v61, v68
	v_exp_f32_e32 v57, v57
	v_mul_f32_e32 v58, 0x3fb8aa3b, v58
	v_exp_f32_e32 v58, v58
	v_mul_f32_e32 v55, 0x3fb8aa3b, v55
	v_exp_f32_e32 v72, v55
	v_cndmask_b32_e64 v60, 0, v57, s[0:1]
	v_sub_f32_e32 v57, v62, v68
	v_add_f32_e32 v56, 0, v70
	v_cndmask_b32_e64 v61, 0, v58, s[0:1]
	v_mul_f32_e32 v57, 0x3fb8aa3b, v57
	v_sub_f32_e32 v58, v63, v68
	v_add_f32_e32 v56, v56, v71
	v_exp_f32_e32 v57, v57
	v_mul_f32_e32 v58, 0x3fb8aa3b, v58
	v_add_f32_e32 v56, v56, v72
	v_exp_f32_e32 v58, v58
	v_add_f32_e32 v56, v56, v59
	v_add_f32_e32 v56, v56, v60
	v_add_f32_e32 v56, v56, v61
	v_cndmask_b32_e64 v62, 0, v57, s[0:1]
	v_add_f32_e32 v56, v56, v62
	v_cndmask_b32_e64 v63, 0, v58, s[0:1]
	v_add_f32_e32 v57, v56, v63
	v_mov_b32_e32 v58, v57
	s_nop 1
	v_permlane16_swap_b32_e32 v57, v58
	v_add_f32_e32 v58, v57, v58
	v_mov_b32_e32 v68, v58
	s_nop 1
	v_permlane32_swap_b32_e32 v58, v68
	v_add_f32_e32 v68, v58, v68
	v_div_scale_f32 v69, s[6:7], v68, v68, 1.0
	v_rcp_f32_e32 v73, v69
	s_nop 0
	v_fma_f32 v75, -v69, v73, 1.0
	v_fmac_f32_e32 v73, v75, v73
	v_div_scale_f32 v75, vcc, 1.0, v68, 1.0
	v_mul_f32_e32 v92, v75, v73
	v_fma_f32 v93, -v69, v92, v75
	v_fmac_f32_e32 v92, v93, v73
	v_fma_f32 v69, -v69, v92, v75
	v_div_fmas_f32 v69, v69, v73, v92
	v_div_fixup_f32 v68, v69, v68, 1.0
	v_mul_f32_e32 v69, v68, v70
	v_mov_b32_e32 v75, 0xbb23d70a
	v_mov_b32_e32 v73, 0x3b23d70a
	v_fmaak_f32 v92, v68, v70, 0xbb23d70a
	v_fmaak_f32 v70, v68, v70, 0x3b23d70a
	v_cmp_lt_f32_e32 vcc, v69, v75
	v_fmaak_f32 v93, v68, v60, 0xbb23d70a
	s_nop 0
	v_cndmask_b32_e32 v70, 0, v70, vcc
	v_cmp_gt_f32_e32 vcc, v69, v73
	s_nop 1
	v_cndmask_b32_e32 v69, v70, v92, vcc
	v_mul_f32_e32 v92, v68, v60
	v_fmaak_f32 v60, v68, v60, 0x3b23d70a
	v_cmp_lt_f32_e32 vcc, v92, v75
	v_max_f32_e32 v70, 0xf149f2ca, v69
	s_nop 0
	v_cndmask_b32_e32 v60, 0, v60, vcc
	v_cmp_gt_f32_e32 vcc, v92, v73
	s_nop 1
	v_cndmask_b32_e32 v92, v60, v93, vcc
	v_max_f32_e32 v60, v70, v92
	v_cndmask_b32_e64 v60, v70, v60, s[0:1]
	v_mul_f32_e32 v70, v68, v71
	v_fmaak_f32 v93, v68, v71, 0xbb23d70a
	v_fmaak_f32 v71, v68, v71, 0x3b23d70a
	v_cmp_lt_f32_e32 vcc, v70, v75
	s_nop 1
	v_cndmask_b32_e32 v71, 0, v71, vcc
	v_cmp_gt_f32_e32 vcc, v70, v73
	s_nop 1
	v_cndmask_b32_e32 v70, v71, v93, vcc
	v_mul_f32_e32 v71, v68, v61
	v_fmaak_f32 v93, v68, v61, 0xbb23d70a
	v_fmaak_f32 v61, v68, v61, 0x3b23d70a
	v_cmp_lt_f32_e32 vcc, v71, v75
	v_max_f32_e32 v60, v60, v70
	s_nop 0
	v_cndmask_b32_e32 v61, 0, v61, vcc
	v_cmp_gt_f32_e32 vcc, v71, v73
	s_nop 1
	v_cndmask_b32_e32 v71, v61, v93, vcc
	v_max_f32_e32 v61, v60, v71
	v_cndmask_b32_e64 v60, v60, v61, s[0:1]
	v_mul_f32_e32 v61, v68, v72
	v_fmaak_f32 v93, v68, v72, 0xbb23d70a
	v_fmaak_f32 v72, v68, v72, 0x3b23d70a
	v_cmp_lt_f32_e32 vcc, v61, v75
	s_nop 1
	v_cndmask_b32_e32 v72, 0, v72, vcc
	v_cmp_gt_f32_e32 vcc, v61, v73
	v_mul_f32_e32 v61, v68, v62
	s_nop 0
	v_cndmask_b32_e32 v72, v72, v93, vcc
	v_fmaak_f32 v93, v68, v62, 0xbb23d70a
	v_fmaak_f32 v62, v68, v62, 0x3b23d70a
	v_cmp_lt_f32_e32 vcc, v61, v75
	v_max_f32_e32 v60, v60, v72
	s_nop 0
	v_cndmask_b32_e32 v62, 0, v62, vcc
	v_cmp_gt_f32_e32 vcc, v61, v73
	s_nop 1
	v_cndmask_b32_e32 v62, v62, v93, vcc
	v_max_f32_e32 v61, v60, v62
	v_cndmask_b32_e64 v60, v60, v61, s[0:1]
	v_mul_f32_e32 v61, v68, v59
	v_fmaak_f32 v93, v68, v59, 0xbb23d70a
	v_fmaak_f32 v59, v68, v59, 0x3b23d70a
	v_cmp_lt_f32_e32 vcc, v61, v75
	s_nop 1
	v_cndmask_b32_e32 v59, 0, v59, vcc
	v_cmp_gt_f32_e32 vcc, v61, v73
	s_nop 1
	v_cndmask_b32_e32 v93, v59, v93, vcc
	v_max_f32_e32 v59, v60, v93
	v_mul_f32_e32 v60, v68, v63
	v_cmp_gt_f32_e32 vcc, v60, v73
	v_fmac_f32_e32 v73, v68, v63
	v_cmp_lt_f32_e64 s[6:7], v60, v75
	v_fmac_f32_e32 v75, v68, v63
	s_nop 0
	v_cndmask_b32_e64 v60, 0, v73, s[6:7]
	v_cndmask_b32_e32 v63, v60, v75, vcc
	v_max_f32_e32 v60, v59, v63
	v_cndmask_b32_e64 v60, v59, v60, s[0:1]
	v_mov_b32_e32 v61, v60
	s_nop 1
	v_permlane16_swap_b32_e32 v60, v61
	v_max_f32_e32 v61, v60, v61
	v_mov_b32_e32 v74, v61
	s_nop 1
	v_permlane32_swap_b32_e32 v61, v74
	v_max_f32_e32 v74, v61, v74
	v_sub_f32_e32 v61, v69, v74
	v_mul_f32_e32 v61, 0x3fb8aa3b, v61
	v_exp_f32_e32 v69, v61
	v_sub_f32_e32 v61, v92, v74
	v_mul_f32_e32 v61, 0x3fb8aa3b, v61
	v_exp_f32_e32 v75, v61
	v_sub_f32_e32 v70, v70, v74
	v_sub_f32_e32 v71, v71, v74
	v_mul_f32_e32 v70, 0x3fb8aa3b, v70
	v_mul_f32_e32 v71, 0x3fb8aa3b, v71
	v_exp_f32_e32 v70, v70
	v_exp_f32_e32 v71, v71
	v_sub_f32_e32 v72, v72, v74
	v_sub_f32_e32 v62, v62, v74
	v_mul_f32_e32 v72, 0x3fb8aa3b, v72
	v_mul_f32_e32 v62, 0x3fb8aa3b, v62
	v_add_f32_e32 v73, 0, v69
	v_cndmask_b32_e64 v75, 0, v75, s[0:1]
	v_exp_f32_e32 v72, v72
	v_exp_f32_e32 v62, v62
	v_sub_f32_e32 v84, v93, v74
	v_sub_f32_e32 v63, v63, v74
	v_add_f32_e32 v73, v73, v75
	v_mul_f32_e32 v84, 0x3fb8aa3b, v84
	v_mul_f32_e32 v63, 0x3fb8aa3b, v63
	v_add_f32_e32 v73, v73, v70
	v_cndmask_b32_e64 v71, 0, v71, s[0:1]
	v_exp_f32_e32 v84, v84
	v_exp_f32_e32 v63, v63
	v_add_f32_e32 v73, v73, v71
	v_add_f32_e32 v73, v73, v72
	v_cndmask_b32_e64 v74, 0, v62, s[0:1]
	v_add_f32_e32 v62, v73, v74
	v_add_f32_e32 v62, v62, v84
	v_cndmask_b32_e64 v73, 0, v63, s[0:1]
	v_add_f32_e32 v85, v62, v73
	v_mov_b32_e32 v66, v85
	s_nop 1
	v_permlane16_swap_b32_e32 v85, v66
	v_add_f32_e32 v66, v85, v66
	v_mov_b32_e32 v67, v66
	s_nop 1
	v_permlane32_swap_b32_e32 v66, v67
	v_add_f32_e32 v66, v66, v67
	v_div_scale_f32 v67, s[6:7], v66, v66, 1.0
	v_rcp_f32_e32 v78, v67
	s_nop 0
	v_fma_f32 v68, -v67, v78, 1.0
	v_fmac_f32_e32 v78, v68, v78
	v_div_scale_f32 v68, vcc, 1.0, v66, 1.0
	v_mul_f32_e32 v77, v68, v78
	v_fma_f32 v79, -v67, v77, v68
	v_fmac_f32_e32 v77, v79, v78
	v_fma_f32 v67, -v67, v77, v68
	v_div_fmas_f32 v67, v67, v78, v77
	v_div_fixup_f32 v66, v67, v66, 1.0
	v_mov_b32_e32 v67, 0xbd4ccccd
	v_fmaak_f32 v68, v66, v69, 0xbd4ccccd
	v_fmaak_f32 v69, v66, v70, 0xbd4ccccd
	v_fmaak_f32 v70, v66, v72, 0xbd4ccccd
	v_fmaak_f32 v75, v66, v75, 0xbd4ccccd
	v_fmaak_f32 v71, v66, v71, 0xbd4ccccd
	v_fmaak_f32 v74, v66, v74, 0xbd4ccccd
	v_mul_f32_e32 v70, 0x4038aa3b, v70
	v_fmaak_f32 v72, v66, v84, 0xbd4ccccd
	v_mul_f32_e32 v75, 0x4038aa3b, v75
	v_mul_f32_e32 v71, 0x4038aa3b, v71
	v_mul_f32_e32 v74, 0x4038aa3b, v74
	v_fmac_f32_e32 v67, v66, v73
	v_mul_f32_e32 v68, 0x4038aa3b, v68
	v_mul_f32_e32 v69, 0x4038aa3b, v69
	v_mul_f32_e32 v72, 0x4038aa3b, v72
	v_cndmask_b32_e64 v75, 0, v75, s[0:1]
	v_cndmask_b32_e64 v71, 0, v71, s[0:1]
	v_cndmask_b32_e64 v74, 0, v74, s[0:1]
	v_mul_f32_e32 v66, 0x4038aa3b, v67
	v_cvt_pk_bf16_f32 v67, v70, v72
	v_add_u32_e32 v70, v76, v198
	v_cndmask_b32_e64 v73, 0, v66, s[0:1]
	v_cndmask_b32_e64 v74, v74, 1.0, s[4:5]
	v_cndmask_b32_e64 v75, v75, 1.0, s[4:5]
	v_cndmask_b32_e64 v71, v71, 1.0, s[4:5]
	v_cvt_pk_bf16_f32 v66, v68, v69
	v_cvt_pk_bf16_f32 v68, v75, v71
	v_cvt_pk_bf16_f32 v69, v74, v73
	ds_write_b128 v70, v[66:69]
	s_movk_i32 s0, 0x210
	v_and_b32_e32 v67, 48, v0
	v_lshrrev_b32_e32 v0, 5, v1
	v_mad_u32_u24 v66, v197, s0, v199
	v_mad_u32_u24 v68, v0, s0, v199
	s_and_b32 s0, s2, 7
	s_lshl_b32 s0, s0, 22
	s_lshl_b32 s1, s3, 17
	v_lshlrev_b32_e32 v1, 13, v0
	s_add_i32 s0, s0, s1
	v_and_b32_e32 v69, 0x1f0, v194
	v_or3_b32 v1, s0, v1, v196
	s_mov_b32 s12, 0
	s_mov_b32 s11, 0x20000
	s_brev_b32 s10, 8
	s_and_b32 s9, s9, 0xffff
	v_or_b32_e32 v0, 0x24800, v198
	v_add_u32_e32 v1, v1, v69
	v_add_u32_e32 v106, v66, v67
	v_add_u32_e32 v107, v68, v69
	s_waitcnt lgkmcnt(0)
	s_barrier
